# sc1 (L1-bypass) on MoE f32 weight loads
# speedup vs baseline: 1.0100x; 1.0021x over previous
.LBB0_1432:
	s_lshr_b32 s33, s2, 6
	s_lshl_b32 s3, s33, 1
	v_or_b32_e32 v2, s3, v193
	s_and_b32 s36, s33, 4
	s_and_b32 s37, s2, 0xc0
	v_and_or_b32 v3, v2, 3, s36
	s_lshr_b32 s36, s2, 1
	s_or_b32 s2, s37, 32
	v_bitop3_b32 v183, s2, v203, v198 bitop3:0xde
	s_or_b32 s2, s37, 0x100
	v_bitop3_b32 v181, s2, v203, v198 bitop3:0xde
	s_or_b32 s2, s37, 0x120
	s_lshl_b32 s38, s33, 10
	v_bitop3_b32 v172, s2, v203, v198 bitop3:0xde
	s_add_i32 s38, s38, 0
	s_mov_b32 s2, m0
	s_mov_b32 m0, s38
	s_nop 0
	global_load_lds_dwordx4 v34, s[18:19]
	s_mov_b32 m0, s2
	s_add_i32 s2, s38, 0x2000
	s_mov_b32 s39, m0
	s_mov_b32 m0, s2
	s_nop 0
	global_load_lds_dwordx4 v35, s[18:19]
	s_mov_b32 m0, s39
	s_add_i32 s2, s38, 0x4000
	s_mov_b32 s39, m0
	s_mov_b32 m0, s2
	s_nop 0
	global_load_lds_dwordx4 v36, s[18:19]
	s_mov_b32 m0, s39
	s_add_i32 s2, s38, 0x6000
	v_lshlrev_b32_e32 v2, 9, v2
	v_lshlrev_b32_e32 v3, 5, v3
	s_and_b32 s36, s36, 0x7fffff80
	s_mov_b32 s39, m0
	s_mov_b32 m0, s2
	s_nop 0
	global_load_lds_dwordx4 v37, s[18:19]
	s_mov_b32 m0, s39
	s_mul_i32 s2, s33, 0x5800
	v_bitop3_b32 v214, v3, v2, v194 bitop3:0xde
	v_or_b32_e32 v2, s36, v1
	s_mul_hi_u32 s39, s3, 0x2c00
	s_add_u32 s40, s59, s2
	s_waitcnt vmcnt(1)
	v_lshlrev_b32_e32 v38, 7, v2
	s_addc_u32 s41, s73, s39
	global_load_dwordx4 v[2:5], v199, s[40:41] sc1
	s_add_i32 s40, s3, 16
	s_add_i32 s83, s2, 0x2c000
	s_mul_hi_u32 s84, s40, 0x2c00
	s_add_u32 s40, s59, s83
	s_addc_u32 s41, s73, s84
	global_load_dwordx4 v[6:9], v199, s[40:41] sc1
	s_add_i32 s40, s3, 32
	s_add_i32 s85, s2, 0x58000
	s_mul_hi_u32 s86, s40, 0x2c00
	s_add_u32 s40, s59, s85
	s_addc_u32 s41, s73, s86
	global_load_dwordx4 v[10:13], v199, s[40:41] sc1
	s_add_i32 s40, s3, 48
	s_add_i32 s87, s2, 0x84000
	s_mul_hi_u32 s88, s40, 0x2c00
	s_add_u32 s40, s59, s87
	s_addc_u32 s41, s73, s88
	global_load_dwordx4 v[14:17], v199, s[40:41] sc1
	s_add_u32 s40, s74, s2
	s_addc_u32 s41, s75, s39
	global_load_dwordx4 v[18:21], v199, s[40:41] sc1
	s_add_u32 s40, s74, s83
	s_addc_u32 s41, s75, s84
	global_load_dwordx4 v[22:25], v199, s[40:41] sc1
	s_add_u32 s40, s74, s85
	s_addc_u32 s41, s75, s86
	global_load_dwordx4 v[26:29], v199, s[40:41] sc1
	s_add_u32 s40, s74, s87
	s_addc_u32 s41, s75, s88
	global_load_dwordx4 v[30:33], v199, s[40:41] sc1
	s_add_i32 s40, s38, 0x8000
	v_add_u32_e32 v39, 0x80, v34
	s_mov_b32 s41, m0
	s_mov_b32 m0, s40
	s_nop 0
	global_load_lds_dwordx4 v39, s[18:19]
	s_mov_b32 m0, s41
	v_add_u32_e32 v39, 0x80, v35
	s_add_i32 s40, s38, 0xa000
	s_mov_b32 s41, m0
	s_mov_b32 m0, s40
	s_nop 0
	global_load_lds_dwordx4 v39, s[18:19]
	s_mov_b32 m0, s41
	v_add_u32_e32 v39, 0x80, v36
	s_add_i32 s40, s38, 0xc000
	s_mov_b32 s41, m0
	s_mov_b32 m0, s40
	s_nop 0
	global_load_lds_dwordx4 v39, s[18:19]
	s_mov_b32 m0, s41
	v_add_u32_e32 v39, 0x80, v37
	s_add_i32 s40, s38, 0xe000
	s_mov_b32 s41, m0
	s_mov_b32 m0, s40
	s_nop 0
	global_load_lds_dwordx4 v39, s[18:19]
	s_mov_b32 m0, s41
	s_waitcnt vmcnt(4)
	v_add_u32_e32 v217, s52, v214
	v_cvt_pk_bf16_f32 v2, v2, v3
	v_cvt_pk_bf16_f32 v3, v4, v5
	v_cvt_pk_bf16_f32 v4, v6, v7
	v_cvt_pk_bf16_f32 v5, v8, v9
	v_or_b32_e32 v213, 0x100, v214
	ds_write2st64_b64 v217, v[2:3], v[4:5] offset1:16
	v_cvt_pk_bf16_f32 v2, v10, v11
	v_cvt_pk_bf16_f32 v3, v12, v13
	v_cvt_pk_bf16_f32 v4, v14, v15
	v_cvt_pk_bf16_f32 v5, v16, v17
	ds_write2st64_b64 v217, v[2:3], v[4:5] offset0:32 offset1:48
	v_cvt_pk_bf16_f32 v2, v18, v19
	v_cvt_pk_bf16_f32 v3, v20, v21
	v_add_u32_e32 v6, s52, v213
	v_cvt_pk_bf16_f32 v4, v22, v23
	v_cvt_pk_bf16_f32 v5, v24, v25
	s_add_i32 s40, s3, 64
	s_add_i32 s83, s2, 0xb0000
	ds_write2st64_b64 v6, v[2:3], v[4:5] offset1:16
	v_cvt_pk_bf16_f32 v2, v26, v27
	v_cvt_pk_bf16_f32 v3, v28, v29
	v_cvt_pk_bf16_f32 v4, v30, v31
	v_cvt_pk_bf16_f32 v5, v32, v33
	s_mul_hi_u32 s84, s40, 0x2c00
	s_add_u32 s40, s59, s83
	ds_write2st64_b64 v6, v[2:3], v[4:5] offset0:32 offset1:48
	s_addc_u32 s41, s73, s84
	global_load_dwordx4 v[30:33], v199, s[40:41] sc1
	s_add_i32 s40, s3, 0x50
	s_add_i32 s85, s2, 0xdc000
	s_mul_hi_u32 s86, s40, 0x2c00
	s_add_u32 s40, s59, s85
	s_addc_u32 s41, s73, s86
	global_load_dwordx4 v[26:29], v199, s[40:41] sc1
	s_add_i32 s40, s3, 0x60
	s_add_i32 s87, s2, 0x108000
	s_mul_hi_u32 s88, s40, 0x2c00
	s_add_u32 s40, s59, s87
	s_addc_u32 s41, s73, s88
	s_addk_i32 s3, 0x70
	s_add_i32 s89, s2, 0x134000
	global_load_dwordx4 v[22:25], v199, s[40:41] sc1
	s_mul_hi_u32 s3, s3, 0x2c00
	s_add_u32 s40, s59, s89
	s_addc_u32 s41, s73, s3
	global_load_dwordx4 v[18:21], v199, s[40:41] sc1
	s_add_u32 s40, s74, s83
	s_addc_u32 s41, s75, s84
	global_load_dwordx4 v[14:17], v199, s[40:41] sc1
	s_add_u32 s40, s74, s85
	s_addc_u32 s41, s75, s86
	global_load_dwordx4 v[10:13], v199, s[40:41] sc1
	s_add_u32 s40, s74, s87
	s_addc_u32 s41, s75, s88
	global_load_dwordx4 v[6:9], v199, s[40:41] sc1
	s_add_u32 s40, s74, s89
	s_addc_u32 s41, s75, s3
	global_load_dwordx4 v[2:5], v199, s[40:41] sc1
	s_mul_hi_u32 s3, s33, 0x5800
	s_add_u32 s40, s74, s2
	s_waitcnt lgkmcnt(0)
	s_barrier
	s_addc_u32 s41, s75, s3
	s_add_u32 s83, s59, s2
	v_add_u32_e32 v221, 0x100, v34
	v_mov_b32_e32 v34, 0
	v_bitop3_b32 v212, s37, v203, v198 bitop3:0xde
	v_or_b32_e32 v215, v38, v196
	s_mov_b32 s39, 0x8000
	v_or_b32_e32 v216, v38, v197
	s_addc_u32 s84, s73, s3
	v_add_u32_e32 v218, 0x100, v37
	v_add_u32_e32 v219, 0x100, v36
	v_add_u32_e32 v220, 0x100, v35
	s_mov_b32 s85, 0x10000
	s_mov_b32 s86, 0
	s_mov_b64 s[2:3], 0
	v_mov_b32_e32 v35, v34
	v_mov_b32_e32 v36, v34
	v_mov_b32_e32 v37, v34
	v_mov_b32_e32 v38, v34
	v_mov_b32_e32 v39, v34
	v_mov_b32_e32 v40, v34
	v_mov_b32_e32 v41, v34
	v_mov_b32_e32 v46, v34
	v_mov_b32_e32 v47, v34
	v_mov_b32_e32 v48, v34
	v_mov_b32_e32 v49, v34
	v_mov_b32_e32 v50, v34
	v_mov_b32_e32 v51, v34
	v_mov_b32_e32 v52, v34
	v_mov_b32_e32 v53, v34
	s_waitcnt vmcnt(0)
	v_mov_b32_e32 v42, v34
	v_mov_b32_e32 v43, v34
	v_mov_b32_e32 v44, v34
	v_mov_b32_e32 v45, v34
	v_mov_b32_e32 v54, v34
	v_mov_b32_e32 v55, v34
	v_mov_b32_e32 v56, v34
	v_mov_b32_e32 v57, v34
	v_mov_b32_e32 v58, v34
	v_mov_b32_e32 v59, v34
	v_mov_b32_e32 v60, v34
	v_mov_b32_e32 v61, v34
	v_mov_b32_e32 v62, v34
	v_mov_b32_e32 v63, v34
	v_mov_b32_e32 v64, v34
	v_mov_b32_e32 v65, v34
	v_mov_b32_e32 v66, v34
	v_mov_b32_e32 v67, v34
	v_mov_b32_e32 v68, v34
	v_mov_b32_e32 v69, v34
	v_mov_b32_e32 v70, v34
	v_mov_b32_e32 v71, v34
	v_mov_b32_e32 v72, v34
	v_mov_b32_e32 v73, v34
	v_mov_b32_e32 v74, v34
	v_mov_b32_e32 v75, v34
	v_mov_b32_e32 v76, v34
	v_mov_b32_e32 v77, v34
	v_mov_b32_e32 v78, v34
	v_mov_b32_e32 v79, v34
	v_mov_b32_e32 v80, v34
	v_mov_b32_e32 v81, v34
	v_mov_b32_e32 v82, v34
	v_mov_b32_e32 v83, v34
	v_mov_b32_e32 v84, v34
	v_mov_b32_e32 v85, v34
	v_mov_b32_e32 v86, v34
	v_mov_b32_e32 v87, v34
	v_mov_b32_e32 v88, v34
	v_mov_b32_e32 v89, v34
	v_mov_b32_e32 v90, v34
	v_mov_b32_e32 v91, v34
	v_mov_b32_e32 v92, v34
	v_mov_b32_e32 v93, v34
	v_mov_b32_e32 v94, v34
	v_mov_b32_e32 v95, v34
	v_mov_b32_e32 v96, v34
	v_mov_b32_e32 v97, v34
	v_mov_b32_e32 v98, v34
	v_mov_b32_e32 v99, v34
	v_mov_b32_e32 v100, v34
	v_mov_b32_e32 v101, v34
	v_mov_b32_e32 v102, v34
	v_mov_b32_e32 v103, v34
	v_mov_b32_e32 v104, v34
	v_mov_b32_e32 v105, v34
	v_mov_b32_e32 v106, v34
	v_mov_b32_e32 v107, v34
	v_mov_b32_e32 v108, v34
	v_mov_b32_e32 v109, v34
	v_mov_b32_e32 v110, v34
	v_mov_b32_e32 v111, v34
	v_mov_b32_e32 v112, v34
	v_mov_b32_e32 v113, v34
	v_mov_b32_e32 v114, v34
	v_mov_b32_e32 v115, v34
	v_mov_b32_e32 v116, v34
	v_mov_b32_e32 v117, v34
	v_mov_b32_e32 v118, v34
	v_mov_b32_e32 v119, v34
	v_mov_b32_e32 v120, v34
	v_mov_b32_e32 v121, v34
	v_mov_b32_e32 v122, v34
	v_mov_b32_e32 v123, v34
	v_mov_b32_e32 v124, v34
	v_mov_b32_e32 v125, v34
	v_mov_b32_e32 v126, v34
	v_mov_b32_e32 v127, v34
	v_mov_b32_e32 v128, v34
	v_mov_b32_e32 v129, v34
	v_mov_b32_e32 v130, v34
	v_mov_b32_e32 v131, v34
	v_mov_b32_e32 v132, v34
	v_mov_b32_e32 v133, v34
	v_mov_b32_e32 v134, v34
	v_mov_b32_e32 v135, v34
	v_mov_b32_e32 v136, v34
	v_mov_b32_e32 v137, v34
	v_mov_b32_e32 v138, v34
	v_mov_b32_e32 v139, v34
	v_mov_b32_e32 v140, v34
	v_mov_b32_e32 v141, v34
	v_mov_b32_e32 v142, v34
	v_mov_b32_e32 v143, v34
	v_mov_b32_e32 v144, v34
	v_mov_b32_e32 v145, v34
	v_mov_b32_e32 v146, v34
	v_mov_b32_e32 v147, v34
	v_mov_b32_e32 v148, v34
	v_mov_b32_e32 v149, v34
	v_mov_b32_e32 v150, v34
	v_mov_b32_e32 v151, v34
	v_mov_b32_e32 v152, v34
	v_mov_b32_e32 v153, v34
	v_mov_b32_e32 v154, v34
	v_mov_b32_e32 v155, v34
	v_mov_b32_e32 v156, v34
	v_mov_b32_e32 v157, v34
	v_mov_b32_e32 v158, v34
	v_mov_b32_e32 v159, v34
	v_mov_b32_e32 v160, v34
	v_mov_b32_e32 v161, v34
.LBB0_1433:
	s_add_i32 s88, s39, 0xffff8000
	s_and_b32 s88, s88, 0x8000
	s_add_i32 s88, s88, 0
	s_add_i32 s87, s86, 0
	s_add_i32 s88, s88, 0x18000
	v_add_u32_e32 v246, s88, v212
	v_add_u32_e32 v247, s87, v215
	v_add_u32_e32 v252, s88, v181
	v_add_u32_e32 v254, s88, v172
	v_add_u32_e32 v250, s88, v183
	ds_read_b64_tr_b16 v[222:223], v246
	ds_read_b64_tr_b16 v[224:225], v246 offset:2048
	ds_read_b64_tr_b16 v[226:227], v250
	ds_read_b64_tr_b16 v[228:229], v250 offset:2048
	ds_read_b128 v[162:165], v247
	ds_read_b128 v[166:169], v247 offset:2048
	ds_read_b64_tr_b16 v[230:231], v252
	ds_read_b64_tr_b16 v[232:233], v252 offset:2048
	ds_read_b64_tr_b16 v[234:235], v254
	ds_read_b64_tr_b16 v[236:237], v254 offset:2048
	s_waitcnt lgkmcnt(5)
	v_mfma_f32_16x16x32_bf16 v[62:65], v[222:225], v[162:165], v[62:65]
	ds_read_b128 v[238:241], v247 offset:4096
	s_and_b32 s88, s39, 0x8000
	s_add_i32 s89, s38, s85
	v_mfma_f32_16x16x32_bf16 v[58:61], v[226:229], v[162:165], v[58:61]
	s_mov_b32 s90, m0
	s_mov_b32 m0, s89
	s_nop 0
	global_load_lds_dwordx4 v221, s[18:19]
	s_mov_b32 m0, s90
	s_waitcnt lgkmcnt(3)
	v_mfma_f32_16x16x32_bf16 v[54:57], v[230:233], v[162:165], v[54:57]
	s_waitcnt lgkmcnt(1)
	v_mfma_f32_16x16x32_bf16 v[42:45], v[234:237], v[162:165], v[42:45]
	v_mfma_f32_16x16x32_bf16 v[50:53], v[222:225], v[166:169], v[50:53]
	ds_read_b128 v[162:165], v247 offset:6144
	s_add_i32 s90, s89, 0x2000
	s_mov_b32 s91, m0
	s_mov_b32 m0, s90
	s_nop 0
	global_load_lds_dwordx4 v220, s[18:19]
	s_mov_b32 m0, s91
	v_mfma_f32_16x16x32_bf16 v[46:49], v[226:229], v[166:169], v[46:49]
	v_mfma_f32_16x16x32_bf16 v[38:41], v[230:233], v[166:169], v[38:41]
	v_mfma_f32_16x16x32_bf16 v[34:37], v[234:237], v[166:169], v[34:37]
	s_waitcnt lgkmcnt(1)
	v_mfma_f32_16x16x32_bf16 v[66:69], v[222:225], v[238:241], v[66:69]
	ds_read_b128 v[166:169], v247 offset:8192
	s_add_i32 s90, s89, 0x4000
	s_mov_b32 s91, m0
	s_mov_b32 m0, s90
	s_nop 0
	global_load_lds_dwordx4 v219, s[18:19]
	s_mov_b32 m0, s91
	v_mfma_f32_16x16x32_bf16 v[70:73], v[226:229], v[238:241], v[70:73]
	v_mfma_f32_16x16x32_bf16 v[74:77], v[230:233], v[238:241], v[74:77]
	v_mfma_f32_16x16x32_bf16 v[78:81], v[234:237], v[238:241], v[78:81]
	s_waitcnt lgkmcnt(1)
	v_mfma_f32_16x16x32_bf16 v[82:85], v[222:225], v[162:165], v[82:85]
	ds_read_b128 v[238:241], v247 offset:10240
	s_addk_i32 s89, 0x6000
	s_mov_b32 s90, m0
	s_mov_b32 m0, s89
	s_nop 0
	global_load_lds_dwordx4 v218, s[18:19]
	s_mov_b32 m0, s90
	v_mfma_f32_16x16x32_bf16 v[86:89], v[226:229], v[162:165], v[86:89]
	v_mfma_f32_16x16x32_bf16 v[90:93], v[230:233], v[162:165], v[90:93]
	v_mfma_f32_16x16x32_bf16 v[94:97], v[234:237], v[162:165], v[94:97]
	ds_read_b128 v[242:245], v247 offset:12288
	ds_read_b64_tr_b16 v[162:163], v246 offset:16384
	ds_read_b64_tr_b16 v[164:165], v246 offset:18432
	s_waitcnt lgkmcnt(4)
	v_mfma_f32_16x16x32_bf16 v[98:101], v[222:225], v[166:169], v[98:101]
	v_mfma_f32_16x16x32_bf16 v[102:105], v[226:229], v[166:169], v[102:105]
	v_mfma_f32_16x16x32_bf16 v[106:109], v[230:233], v[166:169], v[106:109]
	v_mfma_f32_16x16x32_bf16 v[110:113], v[234:237], v[166:169], v[110:113]
	ds_read_b128 v[246:249], v247 offset:14336
	ds_read_b64_tr_b16 v[166:167], v250 offset:16384
	ds_read_b64_tr_b16 v[168:169], v250 offset:18432
	s_waitcnt lgkmcnt(6)
	v_mfma_f32_16x16x32_bf16 v[114:117], v[222:225], v[238:241], v[114:117]
	v_mfma_f32_16x16x32_bf16 v[118:121], v[226:229], v[238:241], v[118:121]
	v_mfma_f32_16x16x32_bf16 v[122:125], v[230:233], v[238:241], v[122:125]
	v_mfma_f32_16x16x32_bf16 v[126:129], v[234:237], v[238:241], v[126:129]
	v_add_u32_e32 v200, s87, v216
	ds_read_b128 v[238:241], v200
	ds_read_b64_tr_b16 v[250:251], v252 offset:16384
	ds_read_b64_tr_b16 v[252:253], v252 offset:18432
	s_waitcnt lgkmcnt(8)
	v_mfma_f32_16x16x32_bf16 v[130:133], v[222:225], v[242:245], v[130:133]
	v_mfma_f32_16x16x32_bf16 v[134:137], v[226:229], v[242:245], v[134:137]
	v_mfma_f32_16x16x32_bf16 v[138:141], v[230:233], v[242:245], v[138:141]
	v_mfma_f32_16x16x32_bf16 v[142:145], v[234:237], v[242:245], v[142:145]
	s_waitcnt lgkmcnt(5)
	v_mfma_f32_16x16x32_bf16 v[146:149], v[222:225], v[246:249], v[146:149]
	v_mfma_f32_16x16x32_bf16 v[150:153], v[226:229], v[246:249], v[150:153]
	ds_read_b128 v[222:225], v200 offset:2048
	ds_read_b64_tr_b16 v[226:227], v254 offset:16384
	ds_read_b64_tr_b16 v[228:229], v254 offset:18432
	v_mfma_f32_16x16x32_bf16 v[154:157], v[230:233], v[246:249], v[154:157]
	v_mfma_f32_16x16x32_bf16 v[158:161], v[234:237], v[246:249], v[158:161]
	ds_read_b128 v[230:233], v200 offset:4096
	s_waitcnt lgkmcnt(6)
	v_mfma_f32_16x16x32_bf16 v[62:65], v[162:165], v[238:241], v[62:65]
	s_add_u32 s87, s83, s2
	s_waitcnt vmcnt(11)
	s_addc_u32 s90, s84, s3
	v_mfma_f32_16x16x32_bf16 v[58:61], v[166:169], v[238:241], v[58:61]
	v_cvt_pk_bf16_f32 v30, v30, v31
	v_cvt_pk_bf16_f32 v31, v32, v33
	v_add_u32_e32 v242, s88, v217
	s_waitcnt lgkmcnt(4)
	v_mfma_f32_16x16x32_bf16 v[54:57], v[250:253], v[238:241], v[54:57]
	s_add_u32 s88, s87, 0x160000
	ds_write_b64 v242, v[30:31]
	s_addc_u32 s89, s90, 0
	s_waitcnt lgkmcnt(2)
	v_mfma_f32_16x16x32_bf16 v[42:45], v[226:229], v[238:241], v[42:45]
	global_load_dwordx4 v[30:33], v199, s[88:89] sc1
	v_mfma_f32_16x16x32_bf16 v[50:53], v[162:165], v[222:225], v[50:53]
	ds_read_b128 v[234:237], v200 offset:6144
	s_waitcnt vmcnt(11)
	s_add_u32 s88, s87, 0x18c000
	v_mfma_f32_16x16x32_bf16 v[46:49], v[166:169], v[222:225], v[46:49]
	v_cvt_pk_bf16_f32 v26, v26, v27
	v_cvt_pk_bf16_f32 v27, v28, v29
	ds_write_b64 v242, v[26:27] offset:8192
	v_mfma_f32_16x16x32_bf16 v[38:41], v[250:253], v[222:225], v[38:41]
	s_addc_u32 s89, s90, 0
	global_load_dwordx4 v[26:29], v199, s[88:89] sc1
	v_mfma_f32_16x16x32_bf16 v[34:37], v[226:229], v[222:225], v[34:37]
	s_waitcnt lgkmcnt(3)
	v_mfma_f32_16x16x32_bf16 v[66:69], v[162:165], v[230:233], v[66:69]
	ds_read_b128 v[222:225], v200 offset:8192
	s_waitcnt vmcnt(11)
	s_add_u32 s88, s87, 0x1b8000
	v_mfma_f32_16x16x32_bf16 v[70:73], v[166:169], v[230:233], v[70:73]
	v_cvt_pk_bf16_f32 v22, v22, v23
	v_cvt_pk_bf16_f32 v23, v24, v25
	ds_write_b64 v242, v[22:23] offset:16384
	v_mfma_f32_16x16x32_bf16 v[74:77], v[250:253], v[230:233], v[74:77]
	s_addc_u32 s89, s90, 0
	global_load_dwordx4 v[22:25], v199, s[88:89] sc1
	v_mfma_f32_16x16x32_bf16 v[78:81], v[226:229], v[230:233], v[78:81]
	s_waitcnt lgkmcnt(3)
	v_mfma_f32_16x16x32_bf16 v[82:85], v[162:165], v[234:237], v[82:85]
	ds_read_b128 v[230:233], v200 offset:10240
	s_waitcnt vmcnt(11)
	s_add_u32 s88, s87, 0x1e4000
	v_mfma_f32_16x16x32_bf16 v[86:89], v[166:169], v[234:237], v[86:89]
	v_cvt_pk_bf16_f32 v18, v18, v19
	v_cvt_pk_bf16_f32 v19, v20, v21
	ds_write_b64 v242, v[18:19] offset:24576
	v_mfma_f32_16x16x32_bf16 v[90:93], v[250:253], v[234:237], v[90:93]
	s_addc_u32 s89, s90, 0
	global_load_dwordx4 v[18:21], v199, s[88:89] sc1
	v_mfma_f32_16x16x32_bf16 v[94:97], v[226:229], v[234:237], v[94:97]
	ds_read_b128 v[234:237], v200 offset:12288
	s_waitcnt lgkmcnt(4)
	v_mfma_f32_16x16x32_bf16 v[98:101], v[162:165], v[222:225], v[98:101]
	s_add_u32 s87, s40, s2
	s_waitcnt vmcnt(11)
	s_addc_u32 s90, s41, s3
	v_mfma_f32_16x16x32_bf16 v[102:105], v[166:169], v[222:225], v[102:105]
	v_cvt_pk_bf16_f32 v14, v14, v15
	v_cvt_pk_bf16_f32 v15, v16, v17
	s_add_u32 s88, s87, 0x160000
	v_mfma_f32_16x16x32_bf16 v[106:109], v[250:253], v[222:225], v[106:109]
	ds_write_b64 v242, v[14:15] offset:256
	s_addc_u32 s89, s90, 0
	global_load_dwordx4 v[14:17], v199, s[88:89] sc1
	v_mfma_f32_16x16x32_bf16 v[110:113], v[226:229], v[222:225], v[110:113]
	s_waitcnt lgkmcnt(3)
	v_mfma_f32_16x16x32_bf16 v[114:117], v[162:165], v[230:233], v[114:117]
	ds_read_b128 v[222:225], v200 offset:14336
	s_waitcnt vmcnt(11)
	s_add_u32 s88, s87, 0x18c000
	v_mfma_f32_16x16x32_bf16 v[118:121], v[166:169], v[230:233], v[118:121]
	v_cvt_pk_bf16_f32 v10, v10, v11
	v_cvt_pk_bf16_f32 v11, v12, v13
	ds_write_b64 v242, v[10:11] offset:8448
	v_mfma_f32_16x16x32_bf16 v[122:125], v[250:253], v[230:233], v[122:125]
	s_addc_u32 s89, s90, 0
	global_load_dwordx4 v[10:13], v199, s[88:89] sc1
	v_mfma_f32_16x16x32_bf16 v[126:129], v[226:229], v[230:233], v[126:129]
	s_waitcnt lgkmcnt(3)
	v_mfma_f32_16x16x32_bf16 v[130:133], v[162:165], v[234:237], v[130:133]
	s_waitcnt vmcnt(11)
	s_add_u32 s88, s87, 0x1b8000
	v_cvt_pk_bf16_f32 v6, v6, v7
	v_mfma_f32_16x16x32_bf16 v[134:137], v[166:169], v[234:237], v[134:137]
	v_cvt_pk_bf16_f32 v7, v8, v9
	ds_write_b64 v242, v[6:7] offset:16640
	s_addc_u32 s89, s90, 0
	v_mfma_f32_16x16x32_bf16 v[138:141], v[250:253], v[234:237], v[138:141]
	global_load_dwordx4 v[6:9], v199, s[88:89] sc1
	v_mfma_f32_16x16x32_bf16 v[142:145], v[226:229], v[234:237], v[142:145]
	s_waitcnt lgkmcnt(2)
	v_mfma_f32_16x16x32_bf16 v[146:149], v[162:165], v[222:225], v[146:149]
	s_waitcnt vmcnt(11)
	s_add_u32 s88, s87, 0x1e4000
	v_cvt_pk_bf16_f32 v2, v2, v3
	v_mfma_f32_16x16x32_bf16 v[150:153], v[166:169], v[222:225], v[150:153]
	v_cvt_pk_bf16_f32 v3, v4, v5
	ds_write_b64 v242, v[2:3] offset:24832
	s_addc_u32 s89, s90, 0
	v_mfma_f32_16x16x32_bf16 v[154:157], v[250:253], v[222:225], v[154:157]
	global_load_dwordx4 v[2:5], v199, s[88:89] sc1
	v_mfma_f32_16x16x32_bf16 v[158:161], v[226:229], v[222:225], v[158:161]
	s_add_i32 s87, s86, 0x8000
	s_cmp_lg_u32 s86, 0x10000
	s_cselect_b32 s86, s87, 0
	s_add_i32 s87, s85, 0x8000
	s_cmp_lg_u32 s85, 0x10000
	s_waitcnt lgkmcnt(0)
	s_barrier
	s_cselect_b32 s85, s87, 0
	s_add_u32 s2, s2, 0xb0000
	s_addc_u32 s3, s3, 0
	s_add_i32 s39, s39, 0x8000
	v_add_u32_e32 v218, 0x80, v218
	v_add_u32_e32 v219, 0x80, v219
	v_add_u32_e32 v220, 0x80, v220
	s_cmp_lg_u32 s2, 0x14a0000
	v_add_u32_e32 v221, 0x80, v221
	s_cbranch_scc1 .LBB0_1433
	v_add_u32_e32 v200, s52, v212
	v_add_u32_e32 v250, 0, v215
	v_add_u32_e32 v215, s52, v181
	v_add_u32_e32 v251, s52, v172
	v_add_u32_e32 v217, s52, v183
	ds_read_b64_tr_b16 v[162:163], v200
	ds_read_b64_tr_b16 v[164:165], v200 offset:2048
	ds_read_b64_tr_b16 v[166:167], v217
	ds_read_b64_tr_b16 v[168:169], v217 offset:2048
	ds_read_b128 v[218:221], v250
	ds_read_b128 v[222:225], v250 offset:2048
	ds_read_b64_tr_b16 v[226:227], v215
	ds_read_b64_tr_b16 v[228:229], v215 offset:2048
	ds_read_b64_tr_b16 v[230:231], v251
	ds_read_b64_tr_b16 v[232:233], v251 offset:2048
	s_waitcnt lgkmcnt(5)
	v_mfma_f32_16x16x32_bf16 v[62:65], v[162:165], v[218:221], v[62:65]
	ds_read_b128 v[234:237], v250 offset:4096
	v_mfma_f32_16x16x32_bf16 v[58:61], v[166:169], v[218:221], v[58:61]
	s_waitcnt lgkmcnt(3)
	v_mfma_f32_16x16x32_bf16 v[54:57], v[226:229], v[218:221], v[54:57]
	s_waitcnt lgkmcnt(1)
	v_mfma_f32_16x16x32_bf16 v[42:45], v[230:233], v[218:221], v[42:45]
	v_mfma_f32_16x16x32_bf16 v[50:53], v[162:165], v[222:225], v[50:53]
	ds_read_b128 v[218:221], v250 offset:6144
	v_mfma_f32_16x16x32_bf16 v[46:49], v[166:169], v[222:225], v[46:49]
	v_mfma_f32_16x16x32_bf16 v[38:41], v[226:229], v[222:225], v[38:41]
	v_mfma_f32_16x16x32_bf16 v[34:37], v[230:233], v[222:225], v[34:37]
	s_waitcnt lgkmcnt(1)
	v_mfma_f32_16x16x32_bf16 v[66:69], v[162:165], v[234:237], v[66:69]
	ds_read_b128 v[222:225], v250 offset:8192
	v_mfma_f32_16x16x32_bf16 v[70:73], v[166:169], v[234:237], v[70:73]
	v_mfma_f32_16x16x32_bf16 v[74:77], v[226:229], v[234:237], v[74:77]
	v_mfma_f32_16x16x32_bf16 v[78:81], v[230:233], v[234:237], v[78:81]
	s_waitcnt lgkmcnt(1)
	v_mfma_f32_16x16x32_bf16 v[82:85], v[162:165], v[218:221], v[82:85]
	ds_read_b128 v[234:237], v250 offset:10240
	v_mfma_f32_16x16x32_bf16 v[86:89], v[166:169], v[218:221], v[86:89]
	v_mfma_f32_16x16x32_bf16 v[90:93], v[226:229], v[218:221], v[90:93]
	v_mfma_f32_16x16x32_bf16 v[94:97], v[230:233], v[218:221], v[94:97]
	ds_read_b128 v[218:221], v250 offset:12288
	ds_read_b64_tr_b16 v[238:239], v200 offset:16384
	ds_read_b64_tr_b16 v[240:241], v200 offset:18432
	s_waitcnt lgkmcnt(4)
	v_mfma_f32_16x16x32_bf16 v[98:101], v[162:165], v[222:225], v[98:101]
	v_mfma_f32_16x16x32_bf16 v[102:105], v[166:169], v[222:225], v[102:105]
	v_mfma_f32_16x16x32_bf16 v[106:109], v[226:229], v[222:225], v[106:109]
	v_mfma_f32_16x16x32_bf16 v[110:113], v[230:233], v[222:225], v[110:113]
	ds_read_b128 v[222:225], v250 offset:14336
	ds_read_b64_tr_b16 v[242:243], v217 offset:16384
	ds_read_b64_tr_b16 v[244:245], v217 offset:18432
	s_waitcnt lgkmcnt(6)
	v_mfma_f32_16x16x32_bf16 v[114:117], v[162:165], v[234:237], v[114:117]
	v_mfma_f32_16x16x32_bf16 v[118:121], v[166:169], v[234:237], v[118:121]
	v_mfma_f32_16x16x32_bf16 v[122:125], v[226:229], v[234:237], v[122:125]
	v_mfma_f32_16x16x32_bf16 v[126:129], v[230:233], v[234:237], v[126:129]
	v_add_u32_e32 v200, 0, v216
	ds_read_b128 v[234:237], v200
	ds_read_b64_tr_b16 v[246:247], v215 offset:16384
	ds_read_b64_tr_b16 v[248:249], v215 offset:18432
	s_waitcnt lgkmcnt(8)
	v_mfma_f32_16x16x32_bf16 v[130:133], v[162:165], v[218:221], v[130:133]
	v_mfma_f32_16x16x32_bf16 v[134:137], v[166:169], v[218:221], v[134:137]
	v_mfma_f32_16x16x32_bf16 v[138:141], v[226:229], v[218:221], v[138:141]
	v_mfma_f32_16x16x32_bf16 v[142:145], v[230:233], v[218:221], v[142:145]
	s_waitcnt lgkmcnt(5)
	v_mfma_f32_16x16x32_bf16 v[146:149], v[162:165], v[222:225], v[146:149]
	v_mfma_f32_16x16x32_bf16 v[150:153], v[166:169], v[222:225], v[150:153]
	ds_read_b128 v[162:165], v200 offset:2048
	ds_read_b64_tr_b16 v[166:167], v251 offset:16384
	ds_read_b64_tr_b16 v[168:169], v251 offset:18432
	v_mfma_f32_16x16x32_bf16 v[154:157], v[226:229], v[222:225], v[154:157]
	v_mfma_f32_16x16x32_bf16 v[158:161], v[230:233], v[222:225], v[158:161]
	ds_read_b128 v[216:219], v200 offset:4096
	s_waitcnt vmcnt(7)
	v_add_u32_e32 v214, s56, v214
	v_cvt_pk_bf16_f32 v30, v30, v31
	v_cvt_pk_bf16_f32 v31, v32, v33
	s_waitcnt lgkmcnt(6)
	v_mfma_f32_16x16x32_bf16 v[62:65], v[238:241], v[234:237], v[62:65]
	ds_write_b64 v214, v[30:31]
	v_mfma_f32_16x16x32_bf16 v[58:61], v[242:245], v[234:237], v[58:61]
	s_waitcnt lgkmcnt(5)
	v_mfma_f32_16x16x32_bf16 v[54:57], v[246:249], v[234:237], v[54:57]
	s_waitcnt lgkmcnt(2)
	v_mfma_f32_16x16x32_bf16 v[30:33], v[166:169], v[234:237], v[42:45]
	v_mfma_f32_16x16x32_bf16 v[42:45], v[238:241], v[162:165], v[50:53]
	s_nop 2
	ds_read_b128 v[50:53], v200 offset:6144
	s_waitcnt vmcnt(6)
	v_mfma_f32_16x16x32_bf16 v[46:49], v[242:245], v[162:165], v[46:49]
	v_cvt_pk_bf16_f32 v26, v26, v27
	v_cvt_pk_bf16_f32 v27, v28, v29
	ds_write_b64 v214, v[26:27] offset:8192
	v_mfma_f32_16x16x32_bf16 v[38:41], v[246:249], v[162:165], v[38:41]
	v_mfma_f32_16x16x32_bf16 v[26:29], v[166:169], v[162:165], v[34:37]
	s_waitcnt lgkmcnt(3)
	v_mfma_f32_16x16x32_bf16 v[34:37], v[238:241], v[216:219], v[66:69]
	v_mfma_f32_16x16x32_bf16 v[66:69], v[242:245], v[216:219], v[70:73]
	s_nop 2
	ds_read_b128 v[70:73], v200 offset:8192
	s_waitcnt vmcnt(5)
	v_mfma_f32_16x16x32_bf16 v[74:77], v[246:249], v[216:219], v[74:77]
	v_cvt_pk_bf16_f32 v22, v22, v23
	v_cvt_pk_bf16_f32 v23, v24, v25
	ds_write_b64 v214, v[22:23] offset:16384
	v_mfma_f32_16x16x32_bf16 v[22:25], v[166:169], v[216:219], v[78:81]
	s_waitcnt lgkmcnt(3)
	v_mfma_f32_16x16x32_bf16 v[78:81], v[238:241], v[50:53], v[82:85]
	v_mfma_f32_16x16x32_bf16 v[82:85], v[242:245], v[50:53], v[86:89]
	s_nop 2
	ds_read_b128 v[86:89], v200 offset:10240
	s_waitcnt vmcnt(4)
	v_mfma_f32_16x16x32_bf16 v[90:93], v[246:249], v[50:53], v[90:93]
	v_cvt_pk_bf16_f32 v18, v18, v19
	v_cvt_pk_bf16_f32 v19, v20, v21
	ds_write_b64 v214, v[18:19] offset:24576
	v_mfma_f32_16x16x32_bf16 v[18:21], v[166:169], v[50:53], v[94:97]
	s_waitcnt lgkmcnt(3)
	v_mfma_f32_16x16x32_bf16 v[50:53], v[238:241], v[70:73], v[98:101]
	v_add_u32_e32 v162, s56, v213
	s_nop 1
	ds_read_b128 v[98:101], v200 offset:12288
	s_waitcnt vmcnt(3)
	v_mfma_f32_16x16x32_bf16 v[94:97], v[242:245], v[70:73], v[102:105]
	v_cvt_pk_bf16_f32 v14, v14, v15
	v_cvt_pk_bf16_f32 v15, v16, v17
	ds_write_b64 v162, v[14:15]
	v_mfma_f32_16x16x32_bf16 v[102:105], v[246:249], v[70:73], v[106:109]
	v_mfma_f32_16x16x32_bf16 v[14:17], v[166:169], v[70:73], v[110:113]
	s_nop 2
	ds_read_b128 v[110:113], v200 offset:14336
	s_waitcnt vmcnt(2)
	s_waitcnt lgkmcnt(4)
	v_mfma_f32_16x16x32_bf16 v[70:73], v[238:241], v[86:89], v[114:117]
	v_cvt_pk_bf16_f32 v10, v10, v11
	v_cvt_pk_bf16_f32 v11, v12, v13
	ds_write_b64 v162, v[10:11] offset:8192
	v_mfma_f32_16x16x32_bf16 v[106:109], v[242:245], v[86:89], v[118:121]
	v_mfma_f32_16x16x32_bf16 v[114:117], v[246:249], v[86:89], v[122:125]
	v_mfma_f32_16x16x32_bf16 v[10:13], v[166:169], v[86:89], v[126:129]
	s_waitcnt vmcnt(1)
	s_waitcnt lgkmcnt(3)
	v_mfma_f32_16x16x32_bf16 v[86:89], v[238:241], v[98:101], v[130:133]
	v_cvt_pk_bf16_f32 v6, v6, v7
	v_cvt_pk_bf16_f32 v7, v8, v9
	ds_write_b64 v162, v[6:7] offset:16384
	v_mfma_f32_16x16x32_bf16 v[118:121], v[242:245], v[98:101], v[134:137]
	v_mfma_f32_16x16x32_bf16 v[122:125], v[246:249], v[98:101], v[138:141]
	v_mfma_f32_16x16x32_bf16 v[6:9], v[166:169], v[98:101], v[142:145]
	s_waitcnt vmcnt(0)
	s_waitcnt lgkmcnt(2)
	v_mfma_f32_16x16x32_bf16 v[98:101], v[238:241], v[110:113], v[146:149]
	v_cvt_pk_bf16_f32 v2, v2, v3
	v_cvt_pk_bf16_f32 v3, v4, v5
	ds_write_b64 v162, v[2:3] offset:24576
	v_mfma_f32_16x16x32_bf16 v[126:129], v[242:245], v[110:113], v[150:153]
	v_mfma_f32_16x16x32_bf16 v[130:133], v[246:249], v[110:113], v[154:157]
	v_mfma_f32_16x16x32_bf16 v[2:5], v[166:169], v[110:113], v[158:161]
	s_waitcnt lgkmcnt(0)
	s_barrier
	v_add_u32_e32 v168, s56, v212
	v_add_u32_e32 v183, s56, v183
	v_add_u32_e32 v181, s56, v181
	ds_read_b64_tr_b16 v[110:111], v168
	ds_read_b64_tr_b16 v[112:113], v168 offset:2048
	ds_read_b64_tr_b16 v[134:135], v183
	ds_read_b64_tr_b16 v[136:137], v183 offset:2048
	ds_read_b128 v[138:141], v250 offset:32768
	ds_read_b64_tr_b16 v[142:143], v181
	ds_read_b128 v[146:149], v250 offset:34816
	ds_read_b128 v[150:153], v250 offset:36864
	ds_read_b64_tr_b16 v[144:145], v181 offset:2048
	v_add_u32_e32 v172, s56, v172
	ds_read_b64_tr_b16 v[154:155], v172
	ds_read_b64_tr_b16 v[156:157], v172 offset:2048
	s_waitcnt lgkmcnt(6)
	v_mfma_f32_16x16x32_bf16 v[62:65], v[110:113], v[138:141], v[62:65]
	v_mfma_f32_16x16x32_bf16 v[58:61], v[134:137], v[138:141], v[58:61]
	s_waitcnt lgkmcnt(2)
	v_mfma_f32_16x16x32_bf16 v[54:57], v[142:145], v[138:141], v[54:57]
	s_waitcnt lgkmcnt(0)
	v_mfma_f32_16x16x32_bf16 v[30:33], v[154:157], v[138:141], v[30:33]
	v_mfma_f32_16x16x32_bf16 v[42:45], v[110:113], v[146:149], v[42:45]
	ds_read_b128 v[138:141], v250 offset:38912
	v_mfma_f32_16x16x32_bf16 v[46:49], v[134:137], v[146:149], v[46:49]
	v_mfma_f32_16x16x32_bf16 v[38:41], v[142:145], v[146:149], v[38:41]
	v_mfma_f32_16x16x32_bf16 v[26:29], v[154:157], v[146:149], v[26:29]
	v_mfma_f32_16x16x32_bf16 v[34:37], v[110:113], v[150:153], v[34:37]
	ds_read_b128 v[146:149], v250 offset:40960
	v_mfma_f32_16x16x32_bf16 v[66:69], v[134:137], v[150:153], v[66:69]
	v_mfma_f32_16x16x32_bf16 v[74:77], v[142:145], v[150:153], v[74:77]
	v_mfma_f32_16x16x32_bf16 v[22:25], v[154:157], v[150:153], v[22:25]
	s_waitcnt lgkmcnt(1)
	v_mfma_f32_16x16x32_bf16 v[150:153], v[134:137], v[138:141], v[82:85]
	s_nop 2
	ds_read_b128 v[82:85], v250 offset:43008
	v_mfma_f32_16x16x32_bf16 v[78:81], v[110:113], v[138:141], v[78:81]
	v_mfma_f32_16x16x32_bf16 v[18:21], v[154:157], v[138:141], v[18:21]
	v_mfma_f32_16x16x32_bf16 v[158:161], v[142:145], v[138:141], v[90:93]
	s_nop 2
	ds_read_b128 v[90:93], v250 offset:45056
	ds_read_b64_tr_b16 v[166:167], v168 offset:16384
	ds_read_b64_tr_b16 v[168:169], v168 offset:18432
	s_waitcnt lgkmcnt(4)
	v_mfma_f32_16x16x32_bf16 v[50:53], v[110:113], v[146:149], v[50:53]
	v_mfma_f32_16x16x32_bf16 v[14:17], v[154:157], v[146:149], v[14:17]
	v_mfma_f32_16x16x32_bf16 v[138:141], v[134:137], v[146:149], v[94:97]
	v_mfma_f32_16x16x32_bf16 v[162:165], v[142:145], v[146:149], v[102:105]
	s_waitcnt lgkmcnt(3)
	v_mfma_f32_16x16x32_bf16 v[146:149], v[110:113], v[82:85], v[70:73]
	s_nop 2
	ds_read_b128 v[70:73], v250 offset:47104
	ds_read_b64_tr_b16 v[220:221], v183 offset:16384
	ds_read_b64_tr_b16 v[222:223], v183 offset:18432
	v_mfma_f32_16x16x32_bf16 v[10:13], v[154:157], v[82:85], v[10:13]
	v_mfma_f32_16x16x32_bf16 v[212:215], v[134:137], v[82:85], v[106:109]
	v_mfma_f32_16x16x32_bf16 v[216:219], v[142:145], v[82:85], v[114:117]
	ds_read_b128 v[82:85], v200 offset:32768
	ds_read_b64_tr_b16 v[236:237], v181 offset:16384
	ds_read_b64_tr_b16 v[238:239], v181 offset:18432
	s_waitcnt lgkmcnt(8)
	v_mfma_f32_16x16x32_bf16 v[6:9], v[154:157], v[90:93], v[6:9]
	v_mfma_f32_16x16x32_bf16 v[224:227], v[110:113], v[90:93], v[86:89]
	v_mfma_f32_16x16x32_bf16 v[228:231], v[134:137], v[90:93], v[118:121]
	v_mfma_f32_16x16x32_bf16 v[232:235], v[142:145], v[90:93], v[122:125]
	s_waitcnt lgkmcnt(5)
	v_mfma_f32_16x16x32_bf16 v[130:133], v[142:145], v[70:73], v[130:133]
	ds_read_b128 v[86:89], v200 offset:34816
	ds_read_b64_tr_b16 v[142:143], v172 offset:16384
	ds_read_b64_tr_b16 v[144:145], v172 offset:18432
	v_mfma_f32_16x16x32_bf16 v[240:243], v[110:113], v[70:73], v[98:101]
	v_mfma_f32_16x16x32_bf16 v[134:137], v[134:137], v[70:73], v[126:129]
	v_mfma_f32_16x16x32_bf16 v[154:157], v[154:157], v[70:73], v[2:5]
	s_nop 2
	ds_read_b128 v[2:5], v200 offset:36864
	s_waitcnt lgkmcnt(6)
	v_mfma_f32_16x16x32_bf16 v[122:125], v[166:169], v[82:85], v[62:65]
	v_mfma_f32_16x16x32_bf16 v[114:117], v[220:223], v[82:85], v[58:61]
	s_waitcnt lgkmcnt(4)
	v_mfma_f32_16x16x32_bf16 v[126:129], v[236:239], v[82:85], v[54:57]
	s_waitcnt lgkmcnt(1)
	v_mfma_f32_16x16x32_bf16 v[118:121], v[142:145], v[82:85], v[30:33]
	s_nop 2
	ds_read_b128 v[30:33], v200 offset:38912
	v_mfma_f32_16x16x32_bf16 v[106:109], v[166:169], v[86:89], v[42:45]
	v_mfma_f32_16x16x32_bf16 v[98:101], v[220:223], v[86:89], v[46:49]
	v_mfma_f32_16x16x32_bf16 v[110:113], v[236:239], v[86:89], v[38:41]
	v_mfma_f32_16x16x32_bf16 v[102:105], v[142:145], v[86:89], v[26:29]
	s_nop 2
	ds_read_b128 v[26:29], v200 offset:40960
	s_waitcnt lgkmcnt(2)
	v_mfma_f32_16x16x32_bf16 v[90:93], v[166:169], v[2:5], v[34:37]
	v_mfma_f32_16x16x32_bf16 v[82:85], v[220:223], v[2:5], v[66:69]
	v_mfma_f32_16x16x32_bf16 v[94:97], v[236:239], v[2:5], v[74:77]
	v_mfma_f32_16x16x32_bf16 v[86:89], v[142:145], v[2:5], v[22:25]
	ds_read_b128 v[2:5], v200 offset:43008
	s_waitcnt lgkmcnt(2)
	v_mfma_f32_16x16x32_bf16 v[74:77], v[166:169], v[30:33], v[78:81]
	v_mfma_f32_16x16x32_bf16 v[66:69], v[220:223], v[30:33], v[150:153]
	v_mfma_f32_16x16x32_bf16 v[78:81], v[236:239], v[30:33], v[158:161]
	v_mfma_f32_16x16x32_bf16 v[70:73], v[142:145], v[30:33], v[18:21]
	ds_read_b128 v[22:25], v200 offset:45056
	s_waitcnt lgkmcnt(2)
	v_mfma_f32_16x16x32_bf16 v[58:61], v[166:169], v[26:29], v[50:53]
	v_mfma_f32_16x16x32_bf16 v[50:53], v[220:223], v[26:29], v[138:141]
	v_mfma_f32_16x16x32_bf16 v[62:65], v[236:239], v[26:29], v[162:165]
	v_mfma_f32_16x16x32_bf16 v[54:57], v[142:145], v[26:29], v[14:17]
	s_waitcnt lgkmcnt(1)
	v_mfma_f32_16x16x32_bf16 v[42:45], v[166:169], v[2:5], v[146:149]
	ds_read_b128 v[138:141], v200 offset:47104
	v_mfma_f32_16x16x32_bf16 v[34:37], v[220:223], v[2:5], v[212:215]
	v_mfma_f32_16x16x32_bf16 v[46:49], v[236:239], v[2:5], v[216:219]
	v_mfma_f32_16x16x32_bf16 v[38:41], v[142:145], v[2:5], v[10:13]
	s_waitcnt lgkmcnt(1)
	v_mfma_f32_16x16x32_bf16 v[26:29], v[166:169], v[22:25], v[224:227]
	v_mfma_f32_16x16x32_bf16 v[18:21], v[220:223], v[22:25], v[228:231]
	v_mfma_f32_16x16x32_bf16 v[30:33], v[236:239], v[22:25], v[232:235]
	v_mfma_f32_16x16x32_bf16 v[22:25], v[142:145], v[22:25], v[6:9]
	s_waitcnt lgkmcnt(0)
	v_mfma_f32_16x16x32_bf16 v[10:13], v[166:169], v[138:141], v[240:243]
	v_mfma_f32_16x16x32_bf16 v[2:5], v[220:223], v[138:141], v[134:137]
	v_mfma_f32_16x16x32_bf16 v[14:17], v[236:239], v[138:141], v[130:133]
	v_mfma_f32_16x16x32_bf16 v[6:9], v[142:145], v[138:141], v[154:157]
	s_waitcnt lgkmcnt(0)
	s_barrier
	s_nop 0
	v_mov_b32_e32 v130, 0
	s_and_b64 vcc, exec, s[6:7]
	v_mov_b32_e32 v131, 0
	v_mov_b32_e32 v132, 0
	s_cbranch_vccnz .LBB0_1436
	global_load_dword v130, v[184:185], off
	global_load_dword v131, v[186:187], off
	global_load_dword v132, v[188:189], off

.LBB0_1539:
	s_ashr_i32 s10, s16, 5
	s_ashr_i32 s11, s10, 31
	s_mul_i32 s14, s10, 0x580000
	s_mul_hi_i32 s2, s10, 0x580000
	s_add_u32 s14, s19, s14
	s_addc_u32 s15, s20, s2
	s_mul_i32 s17, s10, 0x1600000
	s_mul_hi_i32 s2, s10, 0x1600000
	s_add_u32 s17, s64, s17
	s_addc_u32 s2, s65, s2
	s_lshl_b32 s30, s16, 6
	s_and_b32 s30, s30, 0x700
	s_lshl_b32 s31, s30, 2
	s_add_u32 s17, s17, s31
	s_addc_u32 s38, s2, 0
	s_lshl_b32 s2, s16, 8
	v_readfirstlane_b32 s16, v0
	s_and_b32 s31, s2, 0x300
	s_lshr_b32 s2, s16, 6
	s_lshl_b32 s34, s2, 9
	s_lshl_b32 s33, s2, 5
	s_and_b32 s35, s33, 0x60
	v_mov_b32_e32 v3, s34
	s_lshr_b32 s34, s16, 1
	v_bitop3_b32 v206, s35, v3, v194 bitop3:0xde
	s_and_b32 s35, s34, 0x7fffff80
	s_lshl_b32 s34, s16, 1
	s_and_b32 s34, s34, 0x180
	s_or_b32 s36, s34, 32
	v_or_b32_e32 v2, s31, v171
	v_bitop3_b32 v181, s36, v201, v198 bitop3:0xde
	s_or_b32 s36, s34, 64
	v_mul_u32_u24_e32 v34, 0xb00, v2
	v_bitop3_b32 v179, s36, v201, v198 bitop3:0xde
	s_or_b32 s36, s34, 0x60
	v_or_b32_e32 v2, v34, v177
	v_bitop3_b32 v172, s36, v201, v198 bitop3:0xde
	s_lshl_b32 s36, s2, 10
	v_lshlrev_b32_e32 v35, 1, v2
	s_add_i32 s36, s36, 0
	s_mov_b32 s37, m0
	s_mov_b32 m0, s36
	s_nop 0
	global_load_lds_dwordx4 v35, s[14:15]
	s_mov_b32 m0, s37
	s_add_i32 s37, s36, 0x2000
	v_add_lshl_u32 v36, v190, v34, 1
	s_mov_b32 s39, m0
	s_mov_b32 m0, s37
	s_nop 0
	global_load_lds_dwordx4 v36, s[14:15]
	s_mov_b32 m0, s39
	s_add_i32 s37, s36, 0x4000
	v_add_lshl_u32 v37, v191, v34, 1
	s_mov_b32 s39, m0
	s_mov_b32 m0, s37
	s_nop 0
	global_load_lds_dwordx4 v37, s[14:15]
	s_mov_b32 m0, s39
	s_add_i32 s37, s36, 0x6000
	s_lshl_b64 s[40:41], s[2:3], 13
	s_add_u32 s40, s17, s40
	v_bitop3_b32 v2, s33, v194, v203 bitop3:0x6c
	v_or_b32_e32 v4, s35, v1
	s_addc_u32 s41, s38, s41
	s_waitcnt vmcnt(1)
	v_add_lshl_u32 v38, v192, v34, 1
	v_lshlrev_b32_e32 v39, 7, v4
	v_bitop3_b32 v205, v2, s23, v3 bitop3:0x36
	s_mov_b32 s39, m0
	s_mov_b32 m0, s37
	s_nop 0
	global_load_lds_dwordx4 v38, s[14:15]
	s_mov_b32 m0, s39
	global_load_dwordx4 v[2:5], v199, s[40:41] sc1
	s_add_i32 s40, s2, 8
	s_mov_b32 s41, s3
	s_lshl_b64 s[40:41], s[40:41], 13
	s_add_u32 s40, s17, s40
	s_addc_u32 s41, s38, s41
	global_load_dwordx4 v[6:9], v199, s[40:41] sc1
	s_add_i32 s40, s2, 16
	s_mov_b32 s41, s3
	s_lshl_b64 s[40:41], s[40:41], 13
	s_add_u32 s40, s17, s40
	s_addc_u32 s41, s38, s41
	global_load_dwordx4 v[10:13], v199, s[40:41] sc1
	s_add_i32 s40, s2, 24
	s_mov_b32 s41, s3
	s_lshl_b64 s[40:41], s[40:41], 13
	s_add_u32 s40, s17, s40
	s_addc_u32 s41, s38, s41
	global_load_dwordx4 v[14:17], v199, s[40:41] sc1
	s_add_i32 s40, s2, 32
	s_mov_b32 s41, s3
	s_lshl_b64 s[40:41], s[40:41], 13
	s_add_u32 s40, s17, s40
	s_addc_u32 s41, s38, s41
	global_load_dwordx4 v[18:21], v199, s[40:41] sc1
	s_add_i32 s40, s2, 40
	s_mov_b32 s41, s3
	s_lshl_b64 s[40:41], s[40:41], 13
	s_add_u32 s40, s17, s40
	s_addc_u32 s41, s38, s41
	global_load_dwordx4 v[22:25], v199, s[40:41] sc1
	s_add_i32 s40, s2, 48
	s_mov_b32 s41, s3
	s_lshl_b64 s[40:41], s[40:41], 13
	s_add_u32 s40, s17, s40
	s_addc_u32 s41, s38, s41
	global_load_dwordx4 v[26:29], v199, s[40:41] sc1
	s_add_i32 s40, s2, 56
	s_mov_b32 s41, s3
	s_lshl_b64 s[40:41], s[40:41], 13
	s_add_u32 s40, s17, s40
	s_addc_u32 s41, s38, s41
	s_add_i32 s39, s36, 0x8000
	v_or_b32_e32 v35, 0x80, v35
	global_load_dwordx4 v[30:33], v199, s[40:41] sc1
	s_mov_b32 s40, m0
	s_mov_b32 m0, s39
	s_nop 0
	global_load_lds_dwordx4 v35, s[14:15]
	s_mov_b32 m0, s40
	v_or_b32_e32 v35, 0x80, v36
	s_add_i32 s39, s36, 0xa000
	s_mov_b32 s40, m0
	s_mov_b32 m0, s39
	s_nop 0
	global_load_lds_dwordx4 v35, s[14:15]
	s_mov_b32 m0, s40
	v_or_b32_e32 v35, 0x80, v37
	s_add_i32 s39, s36, 0xc000
	s_mov_b32 s40, m0
	s_mov_b32 m0, s39
	s_nop 0
	global_load_lds_dwordx4 v35, s[14:15]
	s_mov_b32 m0, s40
	v_or_b32_e32 v35, 0x80, v38
	s_add_i32 s39, s36, 0xe000
	s_mov_b32 s40, m0
	s_mov_b32 m0, s39
	s_nop 0
	global_load_lds_dwordx4 v35, s[14:15]
	s_mov_b32 m0, s40
	s_waitcnt vmcnt(4)
	s_add_i32 s40, s2, 64
	v_cvt_pk_bf16_f32 v2, v2, v3
	v_cvt_pk_bf16_f32 v3, v4, v5
	v_add_u32_e32 v4, s24, v206
	ds_write_b64 v4, v[2:3]
	v_cvt_pk_bf16_f32 v2, v6, v7
	v_cvt_pk_bf16_f32 v3, v8, v9
	v_add_u32_e32 v5, s24, v205
	ds_write_b64 v5, v[2:3] offset:4096
	v_cvt_pk_bf16_f32 v2, v10, v11
	v_cvt_pk_bf16_f32 v3, v12, v13
	ds_write_b64 v4, v[2:3] offset:8192
	v_cvt_pk_bf16_f32 v2, v14, v15
	v_cvt_pk_bf16_f32 v3, v16, v17
	ds_write_b64 v5, v[2:3] offset:12288
	v_cvt_pk_bf16_f32 v2, v18, v19
	v_cvt_pk_bf16_f32 v3, v20, v21
	s_mov_b32 s41, s3
	ds_write_b64 v4, v[2:3] offset:16384
	v_cvt_pk_bf16_f32 v2, v22, v23
	v_cvt_pk_bf16_f32 v3, v24, v25
	s_lshl_b64 s[40:41], s[40:41], 13
	ds_write_b64 v5, v[2:3] offset:20480
	v_cvt_pk_bf16_f32 v2, v26, v27
	v_cvt_pk_bf16_f32 v3, v28, v29
	s_add_u32 s40, s17, s40
	ds_write_b64 v4, v[2:3] offset:24576
	v_cvt_pk_bf16_f32 v2, v30, v31
	v_cvt_pk_bf16_f32 v3, v32, v33
	s_addc_u32 s41, s38, s41
	ds_write_b64 v5, v[2:3] offset:28672
	global_load_dwordx4 v[30:33], v199, s[40:41] sc1
	s_add_i32 s40, s2, 0x48
	s_mov_b32 s41, s3
	s_lshl_b64 s[40:41], s[40:41], 13
	s_add_u32 s40, s17, s40
	s_addc_u32 s41, s38, s41
	global_load_dwordx4 v[26:29], v199, s[40:41] sc1
	s_add_i32 s40, s2, 0x50
	s_mov_b32 s41, s3
	s_lshl_b64 s[40:41], s[40:41], 13
	s_add_u32 s40, s17, s40
	s_addc_u32 s41, s38, s41
	global_load_dwordx4 v[22:25], v199, s[40:41] sc1
	s_add_i32 s40, s2, 0x58
	s_mov_b32 s41, s3
	s_lshl_b64 s[40:41], s[40:41], 13
	s_add_u32 s40, s17, s40
	s_addc_u32 s41, s38, s41
	global_load_dwordx4 v[18:21], v199, s[40:41] sc1
	s_add_i32 s40, s2, 0x60
	s_mov_b32 s41, s3
	s_lshl_b64 s[40:41], s[40:41], 13
	s_add_u32 s40, s17, s40
	s_addc_u32 s41, s38, s41
	global_load_dwordx4 v[14:17], v199, s[40:41] sc1
	s_add_i32 s40, s2, 0x68
	s_mov_b32 s41, s3
	s_lshl_b64 s[40:41], s[40:41], 13
	s_add_u32 s40, s17, s40
	s_addc_u32 s41, s38, s41
	global_load_dwordx4 v[10:13], v199, s[40:41] sc1
	s_add_i32 s40, s2, 0x70
	s_mov_b32 s41, s3
	s_lshl_b64 s[40:41], s[40:41], 13
	s_add_u32 s40, s17, s40
	s_addc_u32 s41, s38, s41
	s_addk_i32 s2, 0x78
	global_load_dwordx4 v[6:9], v199, s[40:41] sc1
	s_lshl_b64 s[40:41], s[2:3], 13
	s_add_u32 s40, s17, s40
	s_addc_u32 s41, s38, s41
	global_load_dwordx4 v[2:5], v199, s[40:41] sc1
	s_lshl_b64 s[40:41], s[16:17], 7
	s_waitcnt lgkmcnt(0)
	s_barrier
	s_and_b32 s16, s41, 0x7f
	s_and_b32 s2, s40, 0xffffe000
	s_add_u32 s2, s17, s2
	v_lshl_add_u32 v209, v34, 1, v202
	v_mov_b32_e32 v34, 0
	v_bitop3_b32 v183, s34, v201, v198 bitop3:0xde
	v_or_b32_e32 v207, v39, v196
	s_mov_b32 s37, 0x8000
	v_or_b32_e32 v208, v39, v197
	s_addc_u32 s38, s38, s16
	s_mov_b32 s39, 0x10000
	s_mov_b32 s40, 0
	s_mov_b64 s[16:17], 0
	v_mov_b32_e32 v35, v34
	v_mov_b32_e32 v36, v34
	v_mov_b32_e32 v37, v34
	v_mov_b32_e32 v38, v34
	v_mov_b32_e32 v39, v34
	v_mov_b32_e32 v40, v34
	v_mov_b32_e32 v41, v34
	s_waitcnt vmcnt(0)
	v_mov_b32_e32 v42, v34
	v_mov_b32_e32 v43, v34
	v_mov_b32_e32 v44, v34
	v_mov_b32_e32 v45, v34
	v_mov_b32_e32 v46, v34
	v_mov_b32_e32 v47, v34
	v_mov_b32_e32 v48, v34
	v_mov_b32_e32 v49, v34
	v_mov_b32_e32 v50, v34
	v_mov_b32_e32 v51, v34
	v_mov_b32_e32 v52, v34
	v_mov_b32_e32 v53, v34
	v_mov_b32_e32 v54, v34
	v_mov_b32_e32 v55, v34
	v_mov_b32_e32 v56, v34
	v_mov_b32_e32 v57, v34
	v_mov_b32_e32 v58, v34
	v_mov_b32_e32 v59, v34
	v_mov_b32_e32 v60, v34
	v_mov_b32_e32 v61, v34
	v_mov_b32_e32 v62, v34
	v_mov_b32_e32 v63, v34
	v_mov_b32_e32 v64, v34
	v_mov_b32_e32 v65, v34
	v_mov_b32_e32 v66, v34
	v_mov_b32_e32 v67, v34
	v_mov_b32_e32 v68, v34
	v_mov_b32_e32 v69, v34
	v_mov_b32_e32 v70, v34
	v_mov_b32_e32 v71, v34
	v_mov_b32_e32 v72, v34
	v_mov_b32_e32 v73, v34
	v_mov_b32_e32 v74, v34
	v_mov_b32_e32 v75, v34
	v_mov_b32_e32 v76, v34
	v_mov_b32_e32 v77, v34
	v_mov_b32_e32 v78, v34
	v_mov_b32_e32 v79, v34
	v_mov_b32_e32 v80, v34
	v_mov_b32_e32 v81, v34
	v_mov_b32_e32 v82, v34
	v_mov_b32_e32 v83, v34
	v_mov_b32_e32 v84, v34
	v_mov_b32_e32 v85, v34
	v_mov_b32_e32 v86, v34
	v_mov_b32_e32 v87, v34
	v_mov_b32_e32 v88, v34
	v_mov_b32_e32 v89, v34
	v_mov_b32_e32 v90, v34
	v_mov_b32_e32 v91, v34
	v_mov_b32_e32 v92, v34
	v_mov_b32_e32 v93, v34
	v_mov_b32_e32 v94, v34
	v_mov_b32_e32 v95, v34
	v_mov_b32_e32 v96, v34
	v_mov_b32_e32 v97, v34
	v_mov_b32_e32 v98, v34
	v_mov_b32_e32 v99, v34
	v_mov_b32_e32 v100, v34
	v_mov_b32_e32 v101, v34
	v_mov_b32_e32 v102, v34
	v_mov_b32_e32 v103, v34
	v_mov_b32_e32 v104, v34
	v_mov_b32_e32 v105, v34
	v_mov_b32_e32 v106, v34
	v_mov_b32_e32 v107, v34
	v_mov_b32_e32 v108, v34
	v_mov_b32_e32 v109, v34
	v_mov_b32_e32 v110, v34
	v_mov_b32_e32 v111, v34
	v_mov_b32_e32 v112, v34
	v_mov_b32_e32 v113, v34
	v_mov_b32_e32 v114, v34
	v_mov_b32_e32 v115, v34
	v_mov_b32_e32 v116, v34
	v_mov_b32_e32 v117, v34
	v_mov_b32_e32 v118, v34
	v_mov_b32_e32 v119, v34
	v_mov_b32_e32 v120, v34
	v_mov_b32_e32 v121, v34
	v_mov_b32_e32 v122, v34
	v_mov_b32_e32 v123, v34
	v_mov_b32_e32 v124, v34
	v_mov_b32_e32 v125, v34
	v_mov_b32_e32 v126, v34
	v_mov_b32_e32 v127, v34
	v_mov_b32_e32 v128, v34
	v_mov_b32_e32 v129, v34
	v_mov_b32_e32 v130, v34
	v_mov_b32_e32 v131, v34
	v_mov_b32_e32 v132, v34
	v_mov_b32_e32 v133, v34
	v_mov_b32_e32 v134, v34
	v_mov_b32_e32 v135, v34
	v_mov_b32_e32 v136, v34
	v_mov_b32_e32 v137, v34
	v_mov_b32_e32 v138, v34
	v_mov_b32_e32 v139, v34
	v_mov_b32_e32 v140, v34
	v_mov_b32_e32 v141, v34
	v_mov_b32_e32 v142, v34
	v_mov_b32_e32 v143, v34
	v_mov_b32_e32 v144, v34
	v_mov_b32_e32 v145, v34
	v_mov_b32_e32 v146, v34
	v_mov_b32_e32 v147, v34
	v_mov_b32_e32 v148, v34
	v_mov_b32_e32 v149, v34
	v_mov_b32_e32 v150, v34
	v_mov_b32_e32 v151, v34
	v_mov_b32_e32 v152, v34
	v_mov_b32_e32 v153, v34
	v_mov_b32_e32 v158, v34
	v_mov_b32_e32 v159, v34
	v_mov_b32_e32 v160, v34
	v_mov_b32_e32 v161, v34
	v_mov_b32_e32 v154, v34
	v_mov_b32_e32 v155, v34
	v_mov_b32_e32 v156, v34
	v_mov_b32_e32 v157, v34
.LBB0_1540:
	s_add_i32 s42, s37, 0xffff8000
	s_and_b32 s42, s42, 0x8000
	s_add_i32 s41, s40, 0
	s_add_i32 s42, s24, s42
	v_add_u32_e32 v234, s42, v183
	v_add_u32_e32 v235, s41, v207
	v_add_u32_e32 v240, s42, v179
	v_add_u32_e32 v242, s42, v172
	v_add_u32_e32 v238, s42, v181
	ds_read_b64_tr_b16 v[210:211], v234
	ds_read_b64_tr_b16 v[212:213], v234 offset:2048
	ds_read_b64_tr_b16 v[214:215], v238
	ds_read_b64_tr_b16 v[216:217], v238 offset:2048
	ds_read_b128 v[162:165], v235
	ds_read_b128 v[166:169], v235 offset:2048
	ds_read_b64_tr_b16 v[218:219], v240
	ds_read_b64_tr_b16 v[220:221], v240 offset:2048
	ds_read_b64_tr_b16 v[222:223], v242
	ds_read_b64_tr_b16 v[224:225], v242 offset:2048
	s_waitcnt lgkmcnt(5)
	v_mfma_f32_16x16x32_bf16 v[34:37], v[210:213], v[162:165], v[34:37]
	ds_read_b128 v[226:229], v235 offset:4096
	s_and_b32 s42, s37, 0x8000
	v_add_u32_e32 v230, 0xffef8000, v209
	v_mfma_f32_16x16x32_bf16 v[38:41], v[214:217], v[162:165], v[38:41]
	s_add_i32 s43, s36, s39
	s_mov_b32 s44, m0
	s_mov_b32 m0, s43
	s_nop 0
	global_load_lds_dwordx4 v230, s[14:15]
	s_mov_b32 m0, s44
	s_waitcnt lgkmcnt(3)
	v_mfma_f32_16x16x32_bf16 v[42:45], v[218:221], v[162:165], v[42:45]
	s_waitcnt lgkmcnt(1)
	v_mfma_f32_16x16x32_bf16 v[46:49], v[222:225], v[162:165], v[46:49]
	v_mfma_f32_16x16x32_bf16 v[50:53], v[210:213], v[166:169], v[50:53]
	ds_read_b128 v[162:165], v235 offset:6144
	v_add_u32_e32 v230, 0xfff50000, v209
	s_add_i32 s44, s43, 0x2000
	v_mfma_f32_16x16x32_bf16 v[54:57], v[214:217], v[166:169], v[54:57]
	s_mov_b32 s45, m0
	s_mov_b32 m0, s44
	s_nop 0
	global_load_lds_dwordx4 v230, s[14:15]
	s_mov_b32 m0, s45
	v_mfma_f32_16x16x32_bf16 v[58:61], v[218:221], v[166:169], v[58:61]
	v_mfma_f32_16x16x32_bf16 v[62:65], v[222:225], v[166:169], v[62:65]
	s_waitcnt lgkmcnt(1)
	v_mfma_f32_16x16x32_bf16 v[66:69], v[210:213], v[226:229], v[66:69]
	ds_read_b128 v[166:169], v235 offset:8192
	v_add_u32_e32 v230, 0xfffa8000, v209
	s_add_i32 s44, s43, 0x4000
	v_mfma_f32_16x16x32_bf16 v[70:73], v[214:217], v[226:229], v[70:73]
	s_mov_b32 s45, m0
	s_mov_b32 m0, s44
	s_nop 0
	global_load_lds_dwordx4 v230, s[14:15]
	s_mov_b32 m0, s45
	v_mfma_f32_16x16x32_bf16 v[74:77], v[218:221], v[226:229], v[74:77]
	v_mfma_f32_16x16x32_bf16 v[78:81], v[222:225], v[226:229], v[78:81]
	s_waitcnt lgkmcnt(1)
	v_mfma_f32_16x16x32_bf16 v[82:85], v[210:213], v[162:165], v[82:85]
	ds_read_b128 v[226:229], v235 offset:10240
	s_addk_i32 s43, 0x6000
	s_mov_b32 s44, m0
	s_mov_b32 m0, s43
	s_nop 0
	global_load_lds_dwordx4 v209, s[14:15]
	s_mov_b32 m0, s44
	v_mfma_f32_16x16x32_bf16 v[86:89], v[214:217], v[162:165], v[86:89]
	v_mfma_f32_16x16x32_bf16 v[90:93], v[218:221], v[162:165], v[90:93]
	v_mfma_f32_16x16x32_bf16 v[94:97], v[222:225], v[162:165], v[94:97]
	ds_read_b128 v[230:233], v235 offset:12288
	ds_read_b64_tr_b16 v[162:163], v234 offset:16384
	ds_read_b64_tr_b16 v[164:165], v234 offset:18432
	s_waitcnt lgkmcnt(4)
	v_mfma_f32_16x16x32_bf16 v[98:101], v[210:213], v[166:169], v[98:101]
	v_mfma_f32_16x16x32_bf16 v[102:105], v[214:217], v[166:169], v[102:105]
	v_mfma_f32_16x16x32_bf16 v[106:109], v[218:221], v[166:169], v[106:109]
	v_mfma_f32_16x16x32_bf16 v[110:113], v[222:225], v[166:169], v[110:113]
	ds_read_b128 v[234:237], v235 offset:14336
	ds_read_b64_tr_b16 v[166:167], v238 offset:16384
	ds_read_b64_tr_b16 v[168:169], v238 offset:18432
	s_waitcnt lgkmcnt(6)
	v_mfma_f32_16x16x32_bf16 v[114:117], v[210:213], v[226:229], v[114:117]
	v_mfma_f32_16x16x32_bf16 v[118:121], v[214:217], v[226:229], v[118:121]
	v_mfma_f32_16x16x32_bf16 v[122:125], v[218:221], v[226:229], v[122:125]
	v_mfma_f32_16x16x32_bf16 v[126:129], v[222:225], v[226:229], v[126:129]
	v_add_u32_e32 v243, s41, v208
	ds_read_b128 v[226:229], v243
	ds_read_b64_tr_b16 v[238:239], v240 offset:16384
	ds_read_b64_tr_b16 v[240:241], v240 offset:18432
	s_waitcnt lgkmcnt(8)
	v_mfma_f32_16x16x32_bf16 v[130:133], v[210:213], v[230:233], v[130:133]
	v_mfma_f32_16x16x32_bf16 v[134:137], v[214:217], v[230:233], v[134:137]
	v_mfma_f32_16x16x32_bf16 v[138:141], v[218:221], v[230:233], v[138:141]
	v_mfma_f32_16x16x32_bf16 v[142:145], v[222:225], v[230:233], v[142:145]
	s_waitcnt lgkmcnt(5)
	v_mfma_f32_16x16x32_bf16 v[146:149], v[210:213], v[234:237], v[146:149]
	ds_read_b128 v[210:213], v243 offset:2048
	s_add_i32 s41, s24, s42
	v_mfma_f32_16x16x32_bf16 v[150:153], v[214:217], v[234:237], v[150:153]
	ds_read_b64_tr_b16 v[214:215], v242 offset:16384
	ds_read_b64_tr_b16 v[216:217], v242 offset:18432
	v_mfma_f32_16x16x32_bf16 v[158:161], v[218:221], v[234:237], v[158:161]
	v_mfma_f32_16x16x32_bf16 v[154:157], v[222:225], v[234:237], v[154:157]
	ds_read_b128 v[218:221], v243 offset:4096
	s_waitcnt lgkmcnt(6)
	v_mfma_f32_16x16x32_bf16 v[34:37], v[162:165], v[226:229], v[34:37]
	s_add_u32 s44, s2, s16
	s_waitcnt vmcnt(11)
	s_addc_u32 s45, s38, s17
	v_mfma_f32_16x16x32_bf16 v[38:41], v[166:169], v[226:229], v[38:41]
	v_cvt_pk_bf16_f32 v30, v30, v31
	v_cvt_pk_bf16_f32 v31, v32, v33
	v_add_u32_e32 v230, s41, v206
	s_waitcnt lgkmcnt(4)
	v_mfma_f32_16x16x32_bf16 v[42:45], v[238:241], v[226:229], v[42:45]
	s_add_u32 s42, s44, 0x100000
	ds_write_b64 v230, v[30:31]
	s_addc_u32 s43, s45, 0
	s_waitcnt lgkmcnt(2)
	v_mfma_f32_16x16x32_bf16 v[46:49], v[214:217], v[226:229], v[46:49]
	global_load_dwordx4 v[30:33], v199, s[42:43] sc1
	v_mfma_f32_16x16x32_bf16 v[50:53], v[162:165], v[210:213], v[50:53]
	ds_read_b128 v[222:225], v243 offset:6144
	s_waitcnt vmcnt(11)
	v_add_u32_e32 v226, s41, v205
	v_mfma_f32_16x16x32_bf16 v[54:57], v[166:169], v[210:213], v[54:57]
	v_cvt_pk_bf16_f32 v26, v26, v27
	v_cvt_pk_bf16_f32 v27, v28, v29
	s_add_u32 s42, s44, 0x110000
	v_mfma_f32_16x16x32_bf16 v[58:61], v[238:241], v[210:213], v[58:61]
	ds_write_b64 v226, v[26:27] offset:4096
	s_addc_u32 s43, s45, 0
	global_load_dwordx4 v[26:29], v199, s[42:43] sc1
	v_mfma_f32_16x16x32_bf16 v[62:65], v[214:217], v[210:213], v[62:65]
	s_waitcnt lgkmcnt(3)
	v_mfma_f32_16x16x32_bf16 v[66:69], v[162:165], v[218:221], v[66:69]
	ds_read_b128 v[210:213], v243 offset:8192
	s_waitcnt vmcnt(11)
	s_add_u32 s42, s44, 0x120000
	v_mfma_f32_16x16x32_bf16 v[70:73], v[166:169], v[218:221], v[70:73]
	v_cvt_pk_bf16_f32 v22, v22, v23
	v_cvt_pk_bf16_f32 v23, v24, v25
	ds_write_b64 v230, v[22:23] offset:8192
	v_mfma_f32_16x16x32_bf16 v[74:77], v[238:241], v[218:221], v[74:77]
	s_addc_u32 s43, s45, 0
	global_load_dwordx4 v[22:25], v199, s[42:43] sc1
	v_mfma_f32_16x16x32_bf16 v[78:81], v[214:217], v[218:221], v[78:81]
	s_waitcnt lgkmcnt(3)
	v_mfma_f32_16x16x32_bf16 v[82:85], v[162:165], v[222:225], v[82:85]
	ds_read_b128 v[218:221], v243 offset:10240
	s_waitcnt vmcnt(11)
	s_add_u32 s42, s44, 0x130000
	v_mfma_f32_16x16x32_bf16 v[86:89], v[166:169], v[222:225], v[86:89]
	v_cvt_pk_bf16_f32 v18, v18, v19
	v_cvt_pk_bf16_f32 v19, v20, v21
	ds_write_b64 v226, v[18:19] offset:12288
	v_mfma_f32_16x16x32_bf16 v[90:93], v[238:241], v[222:225], v[90:93]
	s_addc_u32 s43, s45, 0
	global_load_dwordx4 v[18:21], v199, s[42:43] sc1
	v_mfma_f32_16x16x32_bf16 v[94:97], v[214:217], v[222:225], v[94:97]
	s_waitcnt lgkmcnt(3)
	v_mfma_f32_16x16x32_bf16 v[98:101], v[162:165], v[210:213], v[98:101]
	ds_read_b128 v[222:225], v243 offset:12288
	s_waitcnt vmcnt(11)
	s_add_u32 s42, s44, 0x140000
	v_mfma_f32_16x16x32_bf16 v[102:105], v[166:169], v[210:213], v[102:105]
	v_cvt_pk_bf16_f32 v14, v14, v15
	v_cvt_pk_bf16_f32 v15, v16, v17
	ds_write_b64 v230, v[14:15] offset:16384
	v_mfma_f32_16x16x32_bf16 v[106:109], v[238:241], v[210:213], v[106:109]
	s_addc_u32 s43, s45, 0
	global_load_dwordx4 v[14:17], v199, s[42:43] sc1
	v_mfma_f32_16x16x32_bf16 v[110:113], v[214:217], v[210:213], v[110:113]
	s_waitcnt lgkmcnt(3)
	v_mfma_f32_16x16x32_bf16 v[114:117], v[162:165], v[218:221], v[114:117]
	ds_read_b128 v[210:213], v243 offset:14336
	s_waitcnt vmcnt(11)
	s_add_u32 s42, s44, 0x150000
	v_mfma_f32_16x16x32_bf16 v[118:121], v[166:169], v[218:221], v[118:121]
	v_cvt_pk_bf16_f32 v10, v10, v11
	v_cvt_pk_bf16_f32 v11, v12, v13
	ds_write_b64 v226, v[10:11] offset:20480
	v_mfma_f32_16x16x32_bf16 v[122:125], v[238:241], v[218:221], v[122:125]
	s_addc_u32 s43, s45, 0
	global_load_dwordx4 v[10:13], v199, s[42:43] sc1
	v_mfma_f32_16x16x32_bf16 v[126:129], v[214:217], v[218:221], v[126:129]
	s_waitcnt lgkmcnt(3)
	v_mfma_f32_16x16x32_bf16 v[130:133], v[162:165], v[222:225], v[130:133]
	s_waitcnt vmcnt(11)
	s_add_u32 s42, s44, 0x160000
	v_cvt_pk_bf16_f32 v6, v6, v7
	v_mfma_f32_16x16x32_bf16 v[134:137], v[166:169], v[222:225], v[134:137]
	v_cvt_pk_bf16_f32 v7, v8, v9
	ds_write_b64 v230, v[6:7] offset:24576
	s_addc_u32 s43, s45, 0
	v_mfma_f32_16x16x32_bf16 v[138:141], v[238:241], v[222:225], v[138:141]
	global_load_dwordx4 v[6:9], v199, s[42:43] sc1
	v_mfma_f32_16x16x32_bf16 v[142:145], v[214:217], v[222:225], v[142:145]
	s_waitcnt lgkmcnt(2)
	v_mfma_f32_16x16x32_bf16 v[146:149], v[162:165], v[210:213], v[146:149]
	s_waitcnt vmcnt(11)
	s_add_u32 s42, s44, 0x170000
	v_cvt_pk_bf16_f32 v2, v2, v3
	v_mfma_f32_16x16x32_bf16 v[150:153], v[166:169], v[210:213], v[150:153]
	v_cvt_pk_bf16_f32 v3, v4, v5
	ds_write_b64 v226, v[2:3] offset:28672
	s_addc_u32 s43, s45, 0
	v_mfma_f32_16x16x32_bf16 v[158:161], v[238:241], v[210:213], v[158:161]
	global_load_dwordx4 v[2:5], v199, s[42:43] sc1
	v_mfma_f32_16x16x32_bf16 v[154:157], v[214:217], v[210:213], v[154:157]
	s_add_i32 s41, s40, 0x8000
	s_cmp_lg_u32 s40, 0x10000
	s_cselect_b32 s40, s41, 0
	s_add_i32 s41, s39, 0x8000
	s_cmp_lg_u32 s39, 0x10000
	s_waitcnt lgkmcnt(0)
	s_barrier
	s_cselect_b32 s39, s41, 0
	s_add_u32 s16, s16, 0x80000
	s_addc_u32 s17, s17, 0
	s_add_i32 s37, s37, 0x8000
	s_cmp_lg_u32 s16, 0x1500000
	v_add_u32_e32 v209, 0x80, v209
	s_cbranch_scc1 .LBB0_1540
	v_add_u32_e32 v209, s24, v183
	v_add_u32_e32 v242, 0, v207
	v_add_u32_e32 v207, s24, v179
	v_add_u32_e32 v243, s24, v172
	v_add_u32_e32 v236, s24, v181
	ds_read_b64_tr_b16 v[162:163], v209
	ds_read_b64_tr_b16 v[164:165], v209 offset:2048
	ds_read_b64_tr_b16 v[166:167], v236
	ds_read_b64_tr_b16 v[168:169], v236 offset:2048
	ds_read_b128 v[210:213], v242
	ds_read_b128 v[214:217], v242 offset:2048
	ds_read_b64_tr_b16 v[218:219], v207
	ds_read_b64_tr_b16 v[220:221], v207 offset:2048
	ds_read_b64_tr_b16 v[222:223], v243
	ds_read_b64_tr_b16 v[224:225], v243 offset:2048
	s_waitcnt lgkmcnt(5)
	v_mfma_f32_16x16x32_bf16 v[34:37], v[162:165], v[210:213], v[34:37]
	ds_read_b128 v[226:229], v242 offset:4096
	v_mfma_f32_16x16x32_bf16 v[38:41], v[166:169], v[210:213], v[38:41]
	s_waitcnt lgkmcnt(3)
	v_mfma_f32_16x16x32_bf16 v[42:45], v[218:221], v[210:213], v[42:45]
	s_waitcnt lgkmcnt(1)
	v_mfma_f32_16x16x32_bf16 v[46:49], v[222:225], v[210:213], v[46:49]
	v_mfma_f32_16x16x32_bf16 v[50:53], v[162:165], v[214:217], v[50:53]
	ds_read_b128 v[210:213], v242 offset:6144
	v_mfma_f32_16x16x32_bf16 v[54:57], v[166:169], v[214:217], v[54:57]
	v_mfma_f32_16x16x32_bf16 v[58:61], v[218:221], v[214:217], v[58:61]
	v_mfma_f32_16x16x32_bf16 v[62:65], v[222:225], v[214:217], v[62:65]
	s_waitcnt lgkmcnt(1)
	v_mfma_f32_16x16x32_bf16 v[66:69], v[162:165], v[226:229], v[66:69]
	ds_read_b128 v[214:217], v242 offset:8192
	v_mfma_f32_16x16x32_bf16 v[70:73], v[166:169], v[226:229], v[70:73]
	v_mfma_f32_16x16x32_bf16 v[74:77], v[218:221], v[226:229], v[74:77]
	v_mfma_f32_16x16x32_bf16 v[78:81], v[222:225], v[226:229], v[78:81]
	s_waitcnt lgkmcnt(1)
	v_mfma_f32_16x16x32_bf16 v[82:85], v[162:165], v[210:213], v[82:85]
	ds_read_b128 v[226:229], v242 offset:10240
	v_mfma_f32_16x16x32_bf16 v[86:89], v[166:169], v[210:213], v[86:89]
	v_mfma_f32_16x16x32_bf16 v[90:93], v[218:221], v[210:213], v[90:93]
	v_mfma_f32_16x16x32_bf16 v[94:97], v[222:225], v[210:213], v[94:97]
	ds_read_b128 v[210:213], v242 offset:12288
	ds_read_b64_tr_b16 v[230:231], v209 offset:16384
	ds_read_b64_tr_b16 v[232:233], v209 offset:18432
	s_waitcnt lgkmcnt(4)
	v_mfma_f32_16x16x32_bf16 v[98:101], v[162:165], v[214:217], v[98:101]
	v_mfma_f32_16x16x32_bf16 v[102:105], v[166:169], v[214:217], v[102:105]
	v_mfma_f32_16x16x32_bf16 v[106:109], v[218:221], v[214:217], v[106:109]
	v_mfma_f32_16x16x32_bf16 v[110:113], v[222:225], v[214:217], v[110:113]
	ds_read_b128 v[214:217], v242 offset:14336
	ds_read_b64_tr_b16 v[234:235], v236 offset:16384
	ds_read_b64_tr_b16 v[236:237], v236 offset:18432
	s_waitcnt lgkmcnt(6)
	v_mfma_f32_16x16x32_bf16 v[114:117], v[162:165], v[226:229], v[114:117]
	v_mfma_f32_16x16x32_bf16 v[118:121], v[166:169], v[226:229], v[118:121]
	v_mfma_f32_16x16x32_bf16 v[122:125], v[218:221], v[226:229], v[122:125]
	v_mfma_f32_16x16x32_bf16 v[126:129], v[222:225], v[226:229], v[126:129]
	v_add_u32_e32 v244, 0, v208
	ds_read_b128 v[226:229], v244
	ds_read_b64_tr_b16 v[238:239], v207 offset:16384
	ds_read_b64_tr_b16 v[240:241], v207 offset:18432
	s_waitcnt lgkmcnt(8)
	v_mfma_f32_16x16x32_bf16 v[130:133], v[162:165], v[210:213], v[130:133]
	v_mfma_f32_16x16x32_bf16 v[134:137], v[166:169], v[210:213], v[134:137]
	v_mfma_f32_16x16x32_bf16 v[138:141], v[218:221], v[210:213], v[138:141]
	v_mfma_f32_16x16x32_bf16 v[142:145], v[222:225], v[210:213], v[142:145]
	s_waitcnt lgkmcnt(5)
	v_mfma_f32_16x16x32_bf16 v[146:149], v[162:165], v[214:217], v[146:149]
	v_mfma_f32_16x16x32_bf16 v[150:153], v[166:169], v[214:217], v[150:153]
	ds_read_b128 v[162:165], v244 offset:2048
	ds_read_b64_tr_b16 v[166:167], v243 offset:16384
	ds_read_b64_tr_b16 v[168:169], v243 offset:18432
	v_mfma_f32_16x16x32_bf16 v[158:161], v[218:221], v[214:217], v[158:161]
	v_mfma_f32_16x16x32_bf16 v[154:157], v[222:225], v[214:217], v[154:157]
	ds_read_b128 v[208:211], v244 offset:4096
	s_waitcnt vmcnt(7)
	v_add_u32_e32 v206, s25, v206
	v_cvt_pk_bf16_f32 v30, v30, v31
	v_cvt_pk_bf16_f32 v31, v32, v33
	s_waitcnt lgkmcnt(6)
	v_mfma_f32_16x16x32_bf16 v[34:37], v[230:233], v[226:229], v[34:37]
	ds_write_b64 v206, v[30:31]
	v_mfma_f32_16x16x32_bf16 v[38:41], v[234:237], v[226:229], v[38:41]
	s_waitcnt lgkmcnt(5)
	v_mfma_f32_16x16x32_bf16 v[42:45], v[238:241], v[226:229], v[42:45]
	s_waitcnt lgkmcnt(2)
	v_mfma_f32_16x16x32_bf16 v[30:33], v[166:169], v[226:229], v[46:49]
	v_mfma_f32_16x16x32_bf16 v[46:49], v[230:233], v[162:165], v[50:53]
	v_add_u32_e32 v205, s25, v205
	v_mfma_f32_16x16x32_bf16 v[50:53], v[234:237], v[162:165], v[54:57]
	s_nop 2
	ds_read_b128 v[54:57], v244 offset:6144
	s_waitcnt vmcnt(6)
	v_mfma_f32_16x16x32_bf16 v[58:61], v[238:241], v[162:165], v[58:61]
	v_cvt_pk_bf16_f32 v26, v26, v27
	v_cvt_pk_bf16_f32 v27, v28, v29
	ds_write_b64 v205, v[26:27] offset:4096
	v_mfma_f32_16x16x32_bf16 v[26:29], v[166:169], v[162:165], v[62:65]
	s_waitcnt lgkmcnt(3)
	v_mfma_f32_16x16x32_bf16 v[62:65], v[230:233], v[208:211], v[66:69]
	v_mfma_f32_16x16x32_bf16 v[66:69], v[234:237], v[208:211], v[70:73]
	s_nop 2
	ds_read_b128 v[70:73], v244 offset:8192
	s_waitcnt vmcnt(5)
	v_mfma_f32_16x16x32_bf16 v[74:77], v[238:241], v[208:211], v[74:77]
	v_cvt_pk_bf16_f32 v22, v22, v23
	v_cvt_pk_bf16_f32 v23, v24, v25
	ds_write_b64 v206, v[22:23] offset:8192
	v_mfma_f32_16x16x32_bf16 v[22:25], v[166:169], v[208:211], v[78:81]
	s_waitcnt lgkmcnt(3)
	v_mfma_f32_16x16x32_bf16 v[78:81], v[230:233], v[54:57], v[82:85]
	v_mfma_f32_16x16x32_bf16 v[82:85], v[234:237], v[54:57], v[86:89]
	s_nop 2
	ds_read_b128 v[86:89], v244 offset:10240
	s_waitcnt vmcnt(4)
	v_mfma_f32_16x16x32_bf16 v[90:93], v[238:241], v[54:57], v[90:93]
	v_cvt_pk_bf16_f32 v18, v18, v19
	v_cvt_pk_bf16_f32 v19, v20, v21
	ds_write_b64 v205, v[18:19] offset:12288
	v_mfma_f32_16x16x32_bf16 v[18:21], v[166:169], v[54:57], v[94:97]
	s_waitcnt lgkmcnt(3)
	v_mfma_f32_16x16x32_bf16 v[54:57], v[230:233], v[70:73], v[98:101]
	s_nop 2
	ds_read_b128 v[98:101], v244 offset:12288
	s_waitcnt vmcnt(3)
	v_mfma_f32_16x16x32_bf16 v[94:97], v[234:237], v[70:73], v[102:105]
	v_cvt_pk_bf16_f32 v14, v14, v15
	v_cvt_pk_bf16_f32 v15, v16, v17
	ds_write_b64 v206, v[14:15] offset:16384
	v_mfma_f32_16x16x32_bf16 v[102:105], v[238:241], v[70:73], v[106:109]
	v_mfma_f32_16x16x32_bf16 v[14:17], v[166:169], v[70:73], v[110:113]
	s_nop 2
	ds_read_b128 v[110:113], v244 offset:14336
	s_waitcnt vmcnt(2)
	s_waitcnt lgkmcnt(4)
	v_mfma_f32_16x16x32_bf16 v[70:73], v[230:233], v[86:89], v[114:117]
	v_cvt_pk_bf16_f32 v10, v10, v11
	v_cvt_pk_bf16_f32 v11, v12, v13
	ds_write_b64 v205, v[10:11] offset:20480
	v_mfma_f32_16x16x32_bf16 v[106:109], v[234:237], v[86:89], v[118:121]
	v_mfma_f32_16x16x32_bf16 v[114:117], v[238:241], v[86:89], v[122:125]
	v_mfma_f32_16x16x32_bf16 v[10:13], v[166:169], v[86:89], v[126:129]
	s_waitcnt vmcnt(1)
	s_waitcnt lgkmcnt(3)
	v_mfma_f32_16x16x32_bf16 v[86:89], v[230:233], v[98:101], v[130:133]
	v_cvt_pk_bf16_f32 v6, v6, v7
	v_cvt_pk_bf16_f32 v7, v8, v9
	ds_write_b64 v206, v[6:7] offset:24576
	v_mfma_f32_16x16x32_bf16 v[118:121], v[234:237], v[98:101], v[134:137]
	v_mfma_f32_16x16x32_bf16 v[122:125], v[238:241], v[98:101], v[138:141]
	v_mfma_f32_16x16x32_bf16 v[6:9], v[166:169], v[98:101], v[142:145]
	s_waitcnt vmcnt(0)
	s_waitcnt lgkmcnt(2)
	v_mfma_f32_16x16x32_bf16 v[98:101], v[230:233], v[110:113], v[146:149]
	v_cvt_pk_bf16_f32 v2, v2, v3
	v_cvt_pk_bf16_f32 v3, v4, v5
	ds_write_b64 v205, v[2:3] offset:28672
	v_mfma_f32_16x16x32_bf16 v[126:129], v[234:237], v[110:113], v[150:153]
	v_mfma_f32_16x16x32_bf16 v[130:133], v[238:241], v[110:113], v[158:161]
	v_mfma_f32_16x16x32_bf16 v[2:5], v[166:169], v[110:113], v[154:157]
	s_waitcnt lgkmcnt(0)
	s_barrier
	v_add_u32_e32 v168, s25, v183
	v_add_u32_e32 v181, s25, v181
	v_add_u32_e32 v179, s25, v179
	ds_read_b64_tr_b16 v[110:111], v168
	ds_read_b64_tr_b16 v[112:113], v168 offset:2048
	ds_read_b64_tr_b16 v[134:135], v181
	ds_read_b64_tr_b16 v[136:137], v181 offset:2048
	ds_read_b128 v[138:141], v242 offset:32768
	ds_read_b64_tr_b16 v[142:143], v179
	ds_read_b128 v[146:149], v242 offset:34816
	ds_read_b128 v[150:153], v242 offset:36864
	ds_read_b64_tr_b16 v[144:145], v179 offset:2048
	v_add_u32_e32 v172, s25, v172
	ds_read_b64_tr_b16 v[154:155], v172
	ds_read_b64_tr_b16 v[156:157], v172 offset:2048
	s_waitcnt lgkmcnt(6)
	v_mfma_f32_16x16x32_bf16 v[34:37], v[110:113], v[138:141], v[34:37]
	v_mfma_f32_16x16x32_bf16 v[38:41], v[134:137], v[138:141], v[38:41]
	s_waitcnt lgkmcnt(2)
	v_mfma_f32_16x16x32_bf16 v[42:45], v[142:145], v[138:141], v[42:45]
	s_waitcnt lgkmcnt(0)
	v_mfma_f32_16x16x32_bf16 v[30:33], v[154:157], v[138:141], v[30:33]
	v_mfma_f32_16x16x32_bf16 v[46:49], v[110:113], v[146:149], v[46:49]
	ds_read_b128 v[138:141], v242 offset:38912
	v_mfma_f32_16x16x32_bf16 v[50:53], v[134:137], v[146:149], v[50:53]
	v_mfma_f32_16x16x32_bf16 v[58:61], v[142:145], v[146:149], v[58:61]
	v_mfma_f32_16x16x32_bf16 v[26:29], v[154:157], v[146:149], v[26:29]
	v_mfma_f32_16x16x32_bf16 v[62:65], v[110:113], v[150:153], v[62:65]
	ds_read_b128 v[146:149], v242 offset:40960
	v_mfma_f32_16x16x32_bf16 v[66:69], v[134:137], v[150:153], v[66:69]
	v_mfma_f32_16x16x32_bf16 v[74:77], v[142:145], v[150:153], v[74:77]
	v_mfma_f32_16x16x32_bf16 v[22:25], v[154:157], v[150:153], v[22:25]
	s_waitcnt lgkmcnt(1)
	v_mfma_f32_16x16x32_bf16 v[150:153], v[134:137], v[138:141], v[82:85]
	s_nop 2
	ds_read_b128 v[82:85], v242 offset:43008
	v_mfma_f32_16x16x32_bf16 v[78:81], v[110:113], v[138:141], v[78:81]
	v_mfma_f32_16x16x32_bf16 v[18:21], v[154:157], v[138:141], v[18:21]
	v_mfma_f32_16x16x32_bf16 v[158:161], v[142:145], v[138:141], v[90:93]
	s_nop 2
	ds_read_b128 v[90:93], v242 offset:45056
	ds_read_b64_tr_b16 v[166:167], v168 offset:16384
	ds_read_b64_tr_b16 v[168:169], v168 offset:18432
	s_waitcnt lgkmcnt(4)
	v_mfma_f32_16x16x32_bf16 v[54:57], v[110:113], v[146:149], v[54:57]
	v_mfma_f32_16x16x32_bf16 v[14:17], v[154:157], v[146:149], v[14:17]
	v_mfma_f32_16x16x32_bf16 v[138:141], v[134:137], v[146:149], v[94:97]
	v_mfma_f32_16x16x32_bf16 v[162:165], v[142:145], v[146:149], v[102:105]
	s_waitcnt lgkmcnt(3)
	v_mfma_f32_16x16x32_bf16 v[146:149], v[110:113], v[82:85], v[70:73]
	s_nop 2
	ds_read_b128 v[70:73], v242 offset:47104
	ds_read_b64_tr_b16 v[214:215], v181 offset:16384
	ds_read_b64_tr_b16 v[216:217], v181 offset:18432
	v_mfma_f32_16x16x32_bf16 v[10:13], v[154:157], v[82:85], v[10:13]
	v_mfma_f32_16x16x32_bf16 v[206:209], v[134:137], v[82:85], v[106:109]
	v_mfma_f32_16x16x32_bf16 v[210:213], v[142:145], v[82:85], v[114:117]
	ds_read_b128 v[82:85], v244 offset:32768
	ds_read_b64_tr_b16 v[230:231], v179 offset:16384
	ds_read_b64_tr_b16 v[232:233], v179 offset:18432
	s_waitcnt lgkmcnt(8)
	v_mfma_f32_16x16x32_bf16 v[6:9], v[154:157], v[90:93], v[6:9]
	v_mfma_f32_16x16x32_bf16 v[218:221], v[110:113], v[90:93], v[86:89]
	v_mfma_f32_16x16x32_bf16 v[222:225], v[134:137], v[90:93], v[118:121]
	v_mfma_f32_16x16x32_bf16 v[226:229], v[142:145], v[90:93], v[122:125]
	s_waitcnt lgkmcnt(5)
	v_mfma_f32_16x16x32_bf16 v[130:133], v[142:145], v[70:73], v[130:133]
	ds_read_b128 v[86:89], v244 offset:34816
	ds_read_b64_tr_b16 v[142:143], v172 offset:16384
	ds_read_b64_tr_b16 v[144:145], v172 offset:18432
	v_mfma_f32_16x16x32_bf16 v[134:137], v[134:137], v[70:73], v[126:129]
	v_mfma_f32_16x16x32_bf16 v[2:5], v[154:157], v[70:73], v[2:5]
	v_mfma_f32_16x16x32_bf16 v[234:237], v[110:113], v[70:73], v[98:101]
	s_waitcnt lgkmcnt(5)
	v_mfma_f32_16x16x32_bf16 v[126:129], v[166:169], v[82:85], v[34:37]
	s_nop 2
	ds_read_b128 v[34:37], v244 offset:36864
	v_mfma_f32_16x16x32_bf16 v[122:125], v[214:217], v[82:85], v[38:41]
	s_waitcnt lgkmcnt(4)
	v_mfma_f32_16x16x32_bf16 v[118:121], v[230:233], v[82:85], v[42:45]
	s_waitcnt lgkmcnt(1)
	v_mfma_f32_16x16x32_bf16 v[114:117], v[142:145], v[82:85], v[30:33]
	s_nop 2
	ds_read_b128 v[30:33], v244 offset:38912
	v_mfma_f32_16x16x32_bf16 v[110:113], v[166:169], v[86:89], v[46:49]
	v_mfma_f32_16x16x32_bf16 v[106:109], v[214:217], v[86:89], v[50:53]
	v_mfma_f32_16x16x32_bf16 v[102:105], v[230:233], v[86:89], v[58:61]
	v_mfma_f32_16x16x32_bf16 v[98:101], v[142:145], v[86:89], v[26:29]
	s_nop 2
	ds_read_b128 v[26:29], v244 offset:40960
	s_waitcnt lgkmcnt(2)
	v_mfma_f32_16x16x32_bf16 v[94:97], v[166:169], v[34:37], v[62:65]
	v_mfma_f32_16x16x32_bf16 v[90:93], v[214:217], v[34:37], v[66:69]
	v_mfma_f32_16x16x32_bf16 v[86:89], v[230:233], v[34:37], v[74:77]
	v_mfma_f32_16x16x32_bf16 v[82:85], v[142:145], v[34:37], v[22:25]
	s_nop 2
	ds_read_b128 v[22:25], v244 offset:43008
	s_waitcnt lgkmcnt(2)
	v_mfma_f32_16x16x32_bf16 v[78:81], v[166:169], v[30:33], v[78:81]
	v_mfma_f32_16x16x32_bf16 v[74:77], v[214:217], v[30:33], v[150:153]
	v_mfma_f32_16x16x32_bf16 v[70:73], v[230:233], v[30:33], v[158:161]
	v_mfma_f32_16x16x32_bf16 v[66:69], v[142:145], v[30:33], v[18:21]
	s_nop 2
	ds_read_b128 v[18:21], v244 offset:45056
	s_waitcnt lgkmcnt(2)
	v_mfma_f32_16x16x32_bf16 v[62:65], v[166:169], v[26:29], v[54:57]
	v_mfma_f32_16x16x32_bf16 v[58:61], v[214:217], v[26:29], v[138:141]
	v_mfma_f32_16x16x32_bf16 v[54:57], v[230:233], v[26:29], v[162:165]
	v_mfma_f32_16x16x32_bf16 v[50:53], v[142:145], v[26:29], v[14:17]
	s_waitcnt lgkmcnt(1)
	v_mfma_f32_16x16x32_bf16 v[46:49], v[166:169], v[22:25], v[146:149]
	ds_read_b128 v[138:141], v244 offset:47104
	v_mfma_f32_16x16x32_bf16 v[42:45], v[214:217], v[22:25], v[206:209]
	v_mfma_f32_16x16x32_bf16 v[38:41], v[230:233], v[22:25], v[210:213]
	v_mfma_f32_16x16x32_bf16 v[34:37], v[142:145], v[22:25], v[10:13]
	s_waitcnt lgkmcnt(1)
	v_mfma_f32_16x16x32_bf16 v[30:33], v[166:169], v[18:21], v[218:221]
	v_mfma_f32_16x16x32_bf16 v[26:29], v[214:217], v[18:21], v[222:225]
	v_mfma_f32_16x16x32_bf16 v[22:25], v[230:233], v[18:21], v[226:229]
	v_mfma_f32_16x16x32_bf16 v[18:21], v[142:145], v[18:21], v[6:9]
	s_waitcnt lgkmcnt(0)
	v_mfma_f32_16x16x32_bf16 v[14:17], v[166:169], v[138:141], v[234:237]
	v_mfma_f32_16x16x32_bf16 v[10:13], v[214:217], v[138:141], v[134:137]
	v_mfma_f32_16x16x32_bf16 v[6:9], v[230:233], v[138:141], v[130:133]
	v_mfma_f32_16x16x32_bf16 v[2:5], v[142:145], v[138:141], v[2:5]
	s_waitcnt lgkmcnt(0)
	s_barrier
	s_nop 0
	v_mov_b32_e32 v131, 0
	s_andn2_b64 vcc, exec, s[12:13]
	v_mov_b32_e32 v133, 0
	v_mov_b32_e32 v134, 0
	s_cbranch_vccnz .LBB0_1536
	global_load_dword v131, v[184:185], off
	global_load_dword v133, v[186:187], off
	global_load_dword v134, v[188:189], off
	s_branch .LBB0_1536
